# speedup vs baseline: 1.0066x; 1.0066x over previous
.LBB7_11:
	s_mov_b64 s[26:27], 0x80
	s_and_b32 s22, s20, 3
	s_add_i32 m0, s43, 0x18000
	v_lshl_add_u64 v[8:9], v[8:9], 0, s[26:27]
	s_lshl_b32 s48, s21, 6
	s_lshl_b32 s21, s21, 13
	s_lshl_b32 s23, s22, 12
	s_waitcnt vmcnt(4)
	s_barrier
	global_load_lds_dwordx4 v[8:9], off
	v_lshl_add_u64 v[6:7], v[6:7], 0, s[26:27]
	s_add_i32 m0, s43, 0x1a000
	s_add_i32 s49, s43, 0x8000
	s_add_i32 s50, s43, 0xa000
	global_load_lds_dwordx4 v[6:7], off
	v_lshl_add_u64 v[4:5], v[4:5], 0, s[26:27]
	s_mov_b32 m0, s49
	s_add_u32 s0, s30, 0xc080
	global_load_lds_dwordx4 v[4:5], off
	v_lshl_add_u64 v[2:3], v[2:3], 0, s[26:27]
	s_mov_b32 m0, s50
	s_addc_u32 s1, s31, 0
	global_load_lds_dwordx4 v[2:3], off
	s_add_i32 m0, s43, 0x1c000
	v_lshl_add_u64 v[2:3], s[0:1], 0, v[146:147]
	global_load_lds_dwordx4 v[2:3], off
	v_lshl_add_u64 v[2:3], s[0:1], 0, v[150:151]
	s_add_i32 m0, s43, 0x1e000
	s_lshl_b32 s53, s33, 2
	global_load_lds_dwordx4 v[2:3], off
	s_abs_i32 s54, s53
	v_cvt_f32_u32_e32 v6, s54
	v_and_b32_e32 v165, 15, v0
	v_and_b32_e32 v2, 48, v0
	v_lshlrev_b32_e32 v4, 2, v0
	v_rcp_iflag_f32_e32 v6, v6
	v_lshlrev_b32_e32 v5, 6, v0
	v_bfe_u32 v167, v0, 3, 3
	v_and_b32_e32 v0, 7, v0
	s_abs_i32 s57, s33
	v_lshlrev_b32_e32 v168, 4, v0
	v_add_lshl_u32 v169, v0, s10, 4
	v_mul_f32_e32 v0, 0x4f7ffffe, v6
	v_cvt_f32_u32_e32 v6, s57
	s_movk_i32 s0, 0x3c0
	s_mulk_i32 s20, 0x900
	v_cvt_u32_f32_e32 v0, v0
	v_rcp_iflag_f32_e32 v6, v6
	v_and_or_b32 v5, v5, s0, v2
	s_add_i32 s0, s20, 0
	v_lshl_or_b32 v3, v165, 6, v2
	v_and_b32_e32 v4, 32, v4
	s_add_i32 s0, s0, 0x20000
	v_bitop3_b32 v3, v3, s21, v4 bitop3:0xde
	v_bitop3_b32 v166, s23, v5, v4 bitop3:0xf6
	s_movk_i32 s1, 0x90
	v_mov_b32_e32 v4, s0
	v_mad_u32_u24 v5, v165, s1, v4
	v_mad_u32_u24 v4, v167, s1, v4
	v_readfirstlane_b32 s1, v0
	v_mul_f32_e32 v0, 0x4f7ffffe, v6
	v_cvt_u32_f32_e32 v0, v0
	s_sub_i32 s0, 0, s54
	s_mul_i32 s0, s0, s1
	s_mul_hi_u32 s0, s1, s0
	s_add_i32 s59, s1, s0
	s_sub_i32 s0, 0, s57
	v_readfirstlane_b32 s1, v0
	s_waitcnt vmcnt(6)
	s_mul_i32 s0, s0, s1
	v_add_u16_e32 v0, v1, v10
	s_mul_hi_u32 s0, s1, s0
	v_lshrrev_b16_e32 v0, 1, v0
	s_add_i32 s65, 0, 0x10000
	s_add_i32 s66, 0, 0x14000
	s_mov_b32 s23, 0x20000
	s_lshl_b32 s51, s22, 6
	s_waitcnt lgkmcnt(0)
	s_ashr_i32 s52, s11, 31
	s_lshl_b32 s22, s10, 17
	s_and_b32 s21, s9, 0xffff
	s_mov_b32 s20, s8
	s_lshl_b32 s55, s10, 5
	s_mul_i32 s56, s10, 48
	s_bfe_i32 s58, s33, 0x1001c
	s_ashr_i32 s60, s33, 31
	s_add_i32 s61, s1, s0
	s_mul_i32 s62, s10, 0xc0
	s_mul_i32 s63, s10, 0x60
	s_lshl_b32 s64, s10, 4
	v_add_lshl_u32 v152, v11, v0, 1
	v_mov_b32_e32 v153, v147
	v_add_lshl_u32 v154, v12, v0, 1
	v_mov_b32_e32 v155, v147
	v_mov_b64_e32 v[156:157], s[6:7]
	v_add_u32_e32 v170, s65, v166
	v_add_u32_e32 v171, 0, v3
	v_add_u32_e32 v172, s66, v166
	v_add_u32_e32 v173, v5, v2
	v_add_u32_e32 v174, v4, v168
	s_barrier
	v_mov_b32_e32 v0, 0
	v_mov_b32_e32 v1, v0
	v_mov_b32_e32 v2, v0
	v_mov_b32_e32 v3, v0
	v_mov_b32_e32 v4, v0
	v_mov_b32_e32 v5, v0
	v_mov_b32_e32 v6, v0
	v_mov_b32_e32 v7, v0
	v_mov_b32_e32 v8, v0
	v_mov_b32_e32 v9, v0
	v_mov_b32_e32 v10, v0
	v_mov_b32_e32 v11, v0
	v_mov_b32_e32 v12, v0
	v_mov_b32_e32 v13, v0
	v_mov_b32_e32 v14, v0
	v_mov_b32_e32 v15, v0
	v_mov_b32_e32 v16, v0
	v_mov_b32_e32 v17, v0
	v_mov_b32_e32 v18, v0
	v_mov_b32_e32 v19, v0
	v_mov_b32_e32 v20, v0
	v_mov_b32_e32 v21, v0
	v_mov_b32_e32 v22, v0
	v_mov_b32_e32 v23, v0
	v_mov_b32_e32 v24, v0
	v_mov_b32_e32 v25, v0
	v_mov_b32_e32 v26, v0
	v_mov_b32_e32 v27, v0
	v_mov_b32_e32 v28, v0
	v_mov_b32_e32 v29, v0
	v_mov_b32_e32 v30, v0
	v_mov_b32_e32 v31, v0
	v_mov_b32_e32 v32, v0
	v_mov_b32_e32 v33, v0
	v_mov_b32_e32 v34, v0
	v_mov_b32_e32 v35, v0
	v_mov_b32_e32 v36, v0
	v_mov_b32_e32 v37, v0
	v_mov_b32_e32 v38, v0
	v_mov_b32_e32 v39, v0
	v_mov_b32_e32 v40, v0
	v_mov_b32_e32 v41, v0
	v_mov_b32_e32 v42, v0
	v_mov_b32_e32 v43, v0
	v_mov_b32_e32 v44, v0
	v_mov_b32_e32 v45, v0
	v_mov_b32_e32 v46, v0
	v_mov_b32_e32 v47, v0
	v_mov_b32_e32 v48, v0
	v_mov_b32_e32 v49, v0
	v_mov_b32_e32 v50, v0
	v_mov_b32_e32 v51, v0
	v_mov_b32_e32 v52, v0
	v_mov_b32_e32 v53, v0
	v_mov_b32_e32 v54, v0
	v_mov_b32_e32 v55, v0
	v_mov_b32_e32 v56, v0
	v_mov_b32_e32 v57, v0
	v_mov_b32_e32 v58, v0
	v_mov_b32_e32 v59, v0
	v_mov_b32_e32 v60, v0
	v_mov_b32_e32 v61, v0
	v_mov_b32_e32 v62, v0
	v_mov_b32_e32 v63, v0
	v_mov_b32_e32 v64, v0
	v_mov_b32_e32 v65, v0
	v_mov_b32_e32 v66, v0
	v_mov_b32_e32 v67, v0
	v_mov_b32_e32 v68, v0
	v_mov_b32_e32 v69, v0
	v_mov_b32_e32 v70, v0
	v_mov_b32_e32 v71, v0
	v_mov_b32_e32 v72, v0
	v_mov_b32_e32 v73, v0
	v_mov_b32_e32 v74, v0
	v_mov_b32_e32 v75, v0
	v_mov_b32_e32 v76, v0
	v_mov_b32_e32 v77, v0
	v_mov_b32_e32 v78, v0
	v_mov_b32_e32 v79, v0
	v_mov_b32_e32 v80, v0
	v_mov_b32_e32 v81, v0
	v_mov_b32_e32 v82, v0
	v_mov_b32_e32 v83, v0
	v_mov_b32_e32 v84, v0
	v_mov_b32_e32 v85, v0
	v_mov_b32_e32 v86, v0
	v_mov_b32_e32 v87, v0
	v_mov_b32_e32 v88, v0
	v_mov_b32_e32 v89, v0
	v_mov_b32_e32 v90, v0
	v_mov_b32_e32 v91, v0
	v_mov_b32_e32 v92, v0
	v_mov_b32_e32 v93, v0
	v_mov_b32_e32 v94, v0
	v_mov_b32_e32 v95, v0
	v_mov_b32_e32 v96, v0
	v_mov_b32_e32 v97, v0
	v_mov_b32_e32 v98, v0
	v_mov_b32_e32 v99, v0
	v_mov_b32_e32 v100, v0
	v_mov_b32_e32 v101, v0
	v_mov_b32_e32 v102, v0
	v_mov_b32_e32 v103, v0
	v_mov_b32_e32 v104, v0
	v_mov_b32_e32 v105, v0
	v_mov_b32_e32 v106, v0
	v_mov_b32_e32 v107, v0
	v_mov_b32_e32 v108, v0
	v_mov_b32_e32 v109, v0
	v_mov_b32_e32 v110, v0
	v_mov_b32_e32 v111, v0
	v_mov_b32_e32 v112, v0
	v_mov_b32_e32 v113, v0
	v_mov_b32_e32 v114, v0
	v_mov_b32_e32 v115, v0
	v_mov_b32_e32 v116, v0
	v_mov_b32_e32 v117, v0
	v_mov_b32_e32 v118, v0
	v_mov_b32_e32 v119, v0
	v_mov_b32_e32 v120, v0
	v_mov_b32_e32 v121, v0
	v_mov_b32_e32 v122, v0
	v_mov_b32_e32 v123, v0
	v_mov_b32_e32 v124, v0
	v_mov_b32_e32 v125, v0
	v_mov_b32_e32 v126, v0
	v_mov_b32_e32 v127, v0

.LBB7_26:
	s_lshl_b32 s34, s70, 8
	s_add_i32 s34, s34, s48
	v_or_b32_e32 v250, s34, v165
	v_ashrrev_i32_e32 v251, 31, v250
	v_lshl_add_u64 v[250:251], v[250:251], 3, s[12:13]
	s_lshl_b32 s35, s67, 8
	s_or_b32 s35, s35, s51
	v_or_b32_e32 v252, s35, v164
	v_ashrrev_i32_e32 v253, 31, v252
	v_lshl_add_u64 v[252:253], v[252:253], 2, s[14:15]
	global_load_dword v226, v[250:251], off offset:4
	global_load_dword v227, v[250:251], off offset:132
	global_load_dword v228, v[250:251], off offset:260
	global_load_dword v229, v[250:251], off offset:388
	global_load_dword v230, v[250:251], off offset:1028
	global_load_dword v231, v[250:251], off offset:1156
	global_load_dword v232, v[250:251], off offset:1284
	global_load_dword v233, v[250:251], off offset:1412
	global_load_dwordx4 v[234:237], v[252:253], off
	global_load_dwordx4 v[238:241], v[252:253], off offset:16
	global_load_dwordx4 v[242:245], v[252:253], off offset:128
	global_load_dwordx4 v[246:249], v[252:253], off offset:144
	s_add_u32 s28, s28, 0x30080
	s_addc_u32 s29, s29, 0
	s_add_u32 s71, s30, 0x100
	v_mov_b32_e32 v0, 0
	s_addc_u32 s72, s31, 0
	s_mov_b32 s73, -2
.LBB7_27:
	ds_read_b128 v[128:131], v170
	ds_read_b128 v[132:135], v170 offset:1024
	ds_read_b128 v[136:139], v170 offset:2048
	ds_read_b128 v[140:143], v170 offset:3072
	s_add_u32 s30, s28, 0xfffd0080
	s_addc_u32 s31, s29, -1
	s_cmp_eq_u32 s73, 8
	s_cselect_b32 s35, s9, s31
	s_cselect_b32 s34, s8, s30
	s_cselect_b32 s31, s1, s72
	s_cselect_b32 s30, s0, s71
	v_lshl_add_u64 v[162:163], s[28:29], 0, v[152:153]
	s_add_i32 m0, s43, 0xc000
	ds_read_b128 v[158:161], v171
	ds_read_b128 v[176:179], v171 offset:1024
	ds_read_b128 v[180:183], v171 offset:2048
	ds_read_b128 v[184:187], v171 offset:3072
	ds_read_b128 v[188:191], v171 offset:4096
	ds_read_b128 v[192:195], v171 offset:5120
	ds_read_b128 v[196:199], v171 offset:6144
	ds_read_b128 v[200:203], v171 offset:7168
	global_load_lds_dwordx4 v[162:163], off
	v_lshl_add_u64 v[162:163], s[28:29], 0, v[154:155]
	s_add_i32 m0, s43, 0xe000
	s_nop 0
	global_load_lds_dwordx4 v[162:163], off
	s_waitcnt lgkmcnt(8)
	s_barrier
	s_waitcnt lgkmcnt(0)
	s_setprio 1
	s_waitcnt lgkmcnt(0)
	v_mfma_f32_16x16x32_f16 v[124:127], v[128:131], v[158:161], v[124:127]
	v_mfma_f32_16x16x32_f16 v[120:123], v[136:139], v[158:161], v[120:123]
	v_mfma_f32_16x16x32_f16 v[108:111], v[128:131], v[180:183], v[108:111]
	v_mfma_f32_16x16x32_f16 v[104:107], v[136:139], v[180:183], v[104:107]
	v_mfma_f32_16x16x32_f16 v[96:99], v[128:131], v[188:191], v[96:99]
	v_mfma_f32_16x16x32_f16 v[88:91], v[136:139], v[188:191], v[88:91]
	v_mfma_f32_16x16x32_f16 v[80:83], v[128:131], v[196:199], v[80:83]
	v_mfma_f32_16x16x32_f16 v[72:75], v[136:139], v[196:199], v[72:75]
	v_mfma_f32_16x16x32_f16 v[124:127], v[132:135], v[176:179], v[124:127]
	v_mfma_f32_16x16x32_f16 v[120:123], v[140:143], v[176:179], v[120:123]
	v_mfma_f32_16x16x32_f16 v[108:111], v[132:135], v[184:187], v[108:111]
	v_mfma_f32_16x16x32_f16 v[104:107], v[140:143], v[184:187], v[104:107]
	v_mfma_f32_16x16x32_f16 v[96:99], v[132:135], v[192:195], v[96:99]
	v_mfma_f32_16x16x32_f16 v[88:91], v[140:143], v[192:195], v[88:91]
	v_mfma_f32_16x16x32_f16 v[80:83], v[132:135], v[200:203], v[80:83]
	v_mfma_f32_16x16x32_f16 v[72:75], v[140:143], v[200:203], v[72:75]
	s_setprio 0
	s_barrier
	s_add_i32 s74, s65, s42
	v_lshl_add_u64 v[162:163], s[30:31], 0, v[146:147]
	s_mov_b32 m0, s74
	ds_read_b128 v[204:207], v172
	ds_read_b128 v[208:211], v172 offset:1024
	ds_read_b128 v[212:215], v172 offset:2048
	ds_read_b128 v[216:219], v172 offset:3072
	global_load_lds_dwordx4 v[162:163], off
	v_lshl_add_u64 v[220:221], s[30:31], 0, v[150:151]
	s_add_i32 m0, s74, 0x2000
	s_nop 0
	global_load_lds_dwordx4 v[220:221], off
	s_barrier
	s_waitcnt lgkmcnt(0)
	s_setprio 1
	s_waitcnt lgkmcnt(0)
	v_mfma_f32_16x16x32_f16 v[116:119], v[204:207], v[158:161], v[116:119]
	v_mfma_f32_16x16x32_f16 v[112:115], v[212:215], v[158:161], v[112:115]
	v_mfma_f32_16x16x32_f16 v[100:103], v[204:207], v[180:183], v[100:103]
	v_mfma_f32_16x16x32_f16 v[92:95], v[212:215], v[180:183], v[92:95]
	v_mfma_f32_16x16x32_f16 v[84:87], v[204:207], v[188:191], v[84:87]
	v_mfma_f32_16x16x32_f16 v[76:79], v[212:215], v[188:191], v[76:79]
	v_mfma_f32_16x16x32_f16 v[68:71], v[204:207], v[196:199], v[68:71]
	v_mfma_f32_16x16x32_f16 v[64:67], v[212:215], v[196:199], v[64:67]
	v_mfma_f32_16x16x32_f16 v[116:119], v[208:211], v[176:179], v[116:119]
	v_mfma_f32_16x16x32_f16 v[112:115], v[216:219], v[176:179], v[112:115]
	v_mfma_f32_16x16x32_f16 v[100:103], v[208:211], v[184:187], v[100:103]
	v_mfma_f32_16x16x32_f16 v[92:95], v[216:219], v[184:187], v[92:95]
	v_mfma_f32_16x16x32_f16 v[84:87], v[208:211], v[192:195], v[84:87]
	v_mfma_f32_16x16x32_f16 v[76:79], v[216:219], v[192:195], v[76:79]
	v_mfma_f32_16x16x32_f16 v[68:71], v[208:211], v[200:203], v[68:71]
	v_mfma_f32_16x16x32_f16 v[64:67], v[216:219], v[200:203], v[64:67]
	s_setprio 0
	s_mov_b32 m0, s43
	v_lshl_add_u64 v[222:223], s[34:35], 0, v[144:145]
	s_barrier
	ds_read_b128 v[158:161], v171 offset:16384
	ds_read_b128 v[176:179], v171 offset:17408
	ds_read_b128 v[180:183], v171 offset:18432
	ds_read_b128 v[184:187], v171 offset:19456
	ds_read_b128 v[188:191], v171 offset:20480
	ds_read_b128 v[192:195], v171 offset:21504
	ds_read_b128 v[196:199], v171 offset:22528
	ds_read_b128 v[200:203], v171 offset:23552
	global_load_lds_dwordx4 v[222:223], off
	v_lshl_add_u64 v[224:225], s[34:35], 0, v[148:149]
	s_mov_b32 m0, s44
	s_nop 0
	global_load_lds_dwordx4 v[224:225], off
	s_barrier
	s_waitcnt lgkmcnt(0)
	s_setprio 1
	s_waitcnt lgkmcnt(0)
	v_mfma_f32_16x16x32_f16 v[60:63], v[128:131], v[158:161], v[60:63]
	v_mfma_f32_16x16x32_f16 v[56:59], v[136:139], v[158:161], v[56:59]
	v_mfma_f32_16x16x32_f16 v[48:51], v[128:131], v[180:183], v[48:51]
	v_mfma_f32_16x16x32_f16 v[40:43], v[136:139], v[180:183], v[40:43]
	v_mfma_f32_16x16x32_f16 v[32:35], v[128:131], v[188:191], v[32:35]
	v_mfma_f32_16x16x32_f16 v[24:27], v[136:139], v[188:191], v[24:27]
	v_mfma_f32_16x16x32_f16 v[16:19], v[128:131], v[196:199], v[16:19]
	v_mfma_f32_16x16x32_f16 v[8:11], v[136:139], v[196:199], v[8:11]
	v_mfma_f32_16x16x32_f16 v[60:63], v[132:135], v[176:179], v[60:63]
	v_mfma_f32_16x16x32_f16 v[56:59], v[140:143], v[176:179], v[56:59]
	v_mfma_f32_16x16x32_f16 v[48:51], v[132:135], v[184:187], v[48:51]
	v_mfma_f32_16x16x32_f16 v[40:43], v[140:143], v[184:187], v[40:43]
	v_mfma_f32_16x16x32_f16 v[32:35], v[132:135], v[192:195], v[32:35]
	v_mfma_f32_16x16x32_f16 v[24:27], v[140:143], v[192:195], v[24:27]
	v_mfma_f32_16x16x32_f16 v[16:19], v[132:135], v[200:203], v[16:19]
	v_mfma_f32_16x16x32_f16 v[8:11], v[140:143], v[200:203], v[8:11]
	s_setprio 0
	s_barrier
	s_add_u32 s74, s30, 0xc000
	s_addc_u32 s75, s31, 0
	s_add_i32 s76, s66, s42
	v_lshl_add_u64 v[128:129], s[74:75], 0, v[146:147]
	s_mov_b32 m0, s76
	s_nop 0
	global_load_lds_dwordx4 v[128:129], off
	v_lshl_add_u64 v[128:129], s[74:75], 0, v[150:151]
	s_add_i32 m0, s76, 0x2000
	s_nop 0
	global_load_lds_dwordx4 v[128:129], off
	s_waitcnt vmcnt(6)
	s_barrier
	s_setprio 1
	v_mfma_f32_16x16x32_f16 v[52:55], v[204:207], v[158:161], v[52:55]
	v_mfma_f32_16x16x32_f16 v[44:47], v[212:215], v[158:161], v[44:47]
	v_mfma_f32_16x16x32_f16 v[36:39], v[204:207], v[180:183], v[36:39]
	v_mfma_f32_16x16x32_f16 v[28:31], v[212:215], v[180:183], v[28:31]
	v_mfma_f32_16x16x32_f16 v[20:23], v[204:207], v[188:191], v[20:23]
	v_mfma_f32_16x16x32_f16 v[12:15], v[212:215], v[188:191], v[12:15]
	v_mfma_f32_16x16x32_f16 v[4:7], v[204:207], v[196:199], v[4:7]
	v_mfma_f32_16x16x32_f16 v[0:3], v[212:215], v[196:199], v[0:3]
	v_mfma_f32_16x16x32_f16 v[52:55], v[208:211], v[176:179], v[52:55]
	v_mfma_f32_16x16x32_f16 v[44:47], v[216:219], v[176:179], v[44:47]
	v_mfma_f32_16x16x32_f16 v[36:39], v[208:211], v[184:187], v[36:39]
	v_mfma_f32_16x16x32_f16 v[28:31], v[216:219], v[184:187], v[28:31]
	v_mfma_f32_16x16x32_f16 v[20:23], v[208:211], v[192:195], v[20:23]
	v_mfma_f32_16x16x32_f16 v[12:15], v[216:219], v[192:195], v[12:15]
	v_mfma_f32_16x16x32_f16 v[4:7], v[208:211], v[200:203], v[4:7]
	v_mfma_f32_16x16x32_f16 v[0:3], v[216:219], v[200:203], v[0:3]
	s_setprio 0
	s_add_i32 s74, 0, 0x18000
	v_add_u32_e32 v140, s74, v166
	s_barrier
	ds_read_b128 v[128:131], v140
	ds_read_b128 v[132:135], v140 offset:1024
	ds_read_b128 v[136:139], v140 offset:2048
	ds_read_b128 v[140:143], v140 offset:3072
	s_add_u32 s34, s34, 0x30000
	s_addc_u32 s35, s35, 0
	s_mov_b32 m0, s45
	v_lshl_add_u64 v[204:205], s[34:35], 0, v[144:145]
	ds_read_b128 v[158:161], v171 offset:32768
	ds_read_b128 v[176:179], v171 offset:33792
	ds_read_b128 v[180:183], v171 offset:34816
	ds_read_b128 v[184:187], v171 offset:35840
	ds_read_b128 v[188:191], v171 offset:36864
	ds_read_b128 v[192:195], v171 offset:37888
	ds_read_b128 v[196:199], v171 offset:38912
	ds_read_b128 v[200:203], v171 offset:39936
	global_load_lds_dwordx4 v[204:205], off
	v_lshl_add_u64 v[204:205], s[34:35], 0, v[148:149]
	s_mov_b32 m0, s46
	s_nop 0
	global_load_lds_dwordx4 v[204:205], off
	s_waitcnt lgkmcnt(8)
	s_barrier
	s_waitcnt lgkmcnt(0)
	s_setprio 1
	s_waitcnt lgkmcnt(0)
	v_mfma_f32_16x16x32_f16 v[124:127], v[128:131], v[158:161], v[124:127]
	v_mfma_f32_16x16x32_f16 v[120:123], v[136:139], v[158:161], v[120:123]
	v_mfma_f32_16x16x32_f16 v[108:111], v[128:131], v[180:183], v[108:111]
	v_mfma_f32_16x16x32_f16 v[104:107], v[136:139], v[180:183], v[104:107]
	v_mfma_f32_16x16x32_f16 v[96:99], v[128:131], v[188:191], v[96:99]
	v_mfma_f32_16x16x32_f16 v[88:91], v[136:139], v[188:191], v[88:91]
	v_mfma_f32_16x16x32_f16 v[80:83], v[128:131], v[196:199], v[80:83]
	v_mfma_f32_16x16x32_f16 v[72:75], v[136:139], v[196:199], v[72:75]
	v_mfma_f32_16x16x32_f16 v[124:127], v[132:135], v[176:179], v[124:127]
	v_mfma_f32_16x16x32_f16 v[120:123], v[140:143], v[176:179], v[120:123]
	v_mfma_f32_16x16x32_f16 v[108:111], v[132:135], v[184:187], v[108:111]
	v_mfma_f32_16x16x32_f16 v[104:107], v[140:143], v[184:187], v[104:107]
	v_mfma_f32_16x16x32_f16 v[96:99], v[132:135], v[192:195], v[96:99]
	v_mfma_f32_16x16x32_f16 v[88:91], v[140:143], v[192:195], v[88:91]
	v_mfma_f32_16x16x32_f16 v[80:83], v[132:135], v[200:203], v[80:83]
	v_mfma_f32_16x16x32_f16 v[72:75], v[140:143], v[200:203], v[72:75]
	s_setprio 0
	s_barrier
	s_add_i32 s34, 0, 0x1c000
	s_add_i32 s35, s74, s42
	v_add_u32_e32 v175, s34, v166
	v_lshl_add_u64 v[162:163], v[162:163], 0, s[26:27]
	s_mov_b32 m0, s35
	ds_read_b128 v[204:207], v175
	ds_read_b128 v[208:211], v175 offset:1024
	ds_read_b128 v[212:215], v175 offset:2048
	ds_read_b128 v[216:219], v175 offset:3072
	global_load_lds_dwordx4 v[162:163], off
	v_lshl_add_u64 v[162:163], v[220:221], 0, s[26:27]
	s_add_i32 m0, s35, 0x2000
	s_nop 0
	global_load_lds_dwordx4 v[162:163], off
	s_barrier
	s_waitcnt lgkmcnt(0)
	s_setprio 1
	s_waitcnt lgkmcnt(0)
	v_mfma_f32_16x16x32_f16 v[116:119], v[204:207], v[158:161], v[116:119]
	v_mfma_f32_16x16x32_f16 v[112:115], v[212:215], v[158:161], v[112:115]
	v_mfma_f32_16x16x32_f16 v[100:103], v[204:207], v[180:183], v[100:103]
	v_mfma_f32_16x16x32_f16 v[92:95], v[212:215], v[180:183], v[92:95]
	v_mfma_f32_16x16x32_f16 v[84:87], v[204:207], v[188:191], v[84:87]
	v_mfma_f32_16x16x32_f16 v[76:79], v[212:215], v[188:191], v[76:79]
	v_mfma_f32_16x16x32_f16 v[68:71], v[204:207], v[196:199], v[68:71]
	v_mfma_f32_16x16x32_f16 v[64:67], v[212:215], v[196:199], v[64:67]
	v_mfma_f32_16x16x32_f16 v[116:119], v[208:211], v[176:179], v[116:119]
	v_mfma_f32_16x16x32_f16 v[112:115], v[216:219], v[176:179], v[112:115]
	v_mfma_f32_16x16x32_f16 v[100:103], v[208:211], v[184:187], v[100:103]
	v_mfma_f32_16x16x32_f16 v[92:95], v[216:219], v[184:187], v[92:95]
	v_mfma_f32_16x16x32_f16 v[84:87], v[208:211], v[192:195], v[84:87]
	v_mfma_f32_16x16x32_f16 v[76:79], v[216:219], v[192:195], v[76:79]
	v_mfma_f32_16x16x32_f16 v[68:71], v[208:211], v[200:203], v[68:71]
	v_mfma_f32_16x16x32_f16 v[64:67], v[216:219], v[200:203], v[64:67]
	s_setprio 0
	s_mov_b32 m0, s49
	v_lshl_add_u64 v[162:163], v[222:223], 0, s[26:27]
	s_barrier
	ds_read_b128 v[158:161], v171 offset:49152
	ds_read_b128 v[176:179], v171 offset:50176
	ds_read_b128 v[180:183], v171 offset:51200
	ds_read_b128 v[184:187], v171 offset:52224
	ds_read_b128 v[188:191], v171 offset:53248
	ds_read_b128 v[192:195], v171 offset:54272
	ds_read_b128 v[196:199], v171 offset:55296
	ds_read_b128 v[200:203], v171 offset:56320
	global_load_lds_dwordx4 v[162:163], off
	v_lshl_add_u64 v[162:163], v[224:225], 0, s[26:27]
	s_mov_b32 m0, s50
	s_nop 0
	global_load_lds_dwordx4 v[162:163], off
	s_barrier
	s_waitcnt lgkmcnt(0)
	s_setprio 1
	s_waitcnt lgkmcnt(0)
	v_mfma_f32_16x16x32_f16 v[60:63], v[128:131], v[158:161], v[60:63]
	v_mfma_f32_16x16x32_f16 v[56:59], v[136:139], v[158:161], v[56:59]
	v_mfma_f32_16x16x32_f16 v[48:51], v[128:131], v[180:183], v[48:51]
	v_mfma_f32_16x16x32_f16 v[40:43], v[136:139], v[180:183], v[40:43]
	v_mfma_f32_16x16x32_f16 v[32:35], v[128:131], v[188:191], v[32:35]
	v_mfma_f32_16x16x32_f16 v[24:27], v[136:139], v[188:191], v[24:27]
	v_mfma_f32_16x16x32_f16 v[16:19], v[128:131], v[196:199], v[16:19]
	v_mfma_f32_16x16x32_f16 v[8:11], v[136:139], v[196:199], v[8:11]
	v_mfma_f32_16x16x32_f16 v[60:63], v[132:135], v[176:179], v[60:63]
	v_mfma_f32_16x16x32_f16 v[56:59], v[140:143], v[176:179], v[56:59]
	v_mfma_f32_16x16x32_f16 v[48:51], v[132:135], v[184:187], v[48:51]
	v_mfma_f32_16x16x32_f16 v[40:43], v[140:143], v[184:187], v[40:43]
	v_mfma_f32_16x16x32_f16 v[32:35], v[132:135], v[192:195], v[32:35]
	v_mfma_f32_16x16x32_f16 v[24:27], v[140:143], v[192:195], v[24:27]
	v_mfma_f32_16x16x32_f16 v[16:19], v[132:135], v[200:203], v[16:19]
	v_mfma_f32_16x16x32_f16 v[8:11], v[140:143], v[200:203], v[8:11]
	s_setprio 0
	s_barrier
	s_add_u32 s30, s30, 0xc080
	s_addc_u32 s31, s31, 0
	s_add_i32 s34, s34, s42
	v_lshl_add_u64 v[128:129], s[30:31], 0, v[146:147]
	s_mov_b32 m0, s34
	s_nop 0
	global_load_lds_dwordx4 v[128:129], off
	v_lshl_add_u64 v[128:129], s[30:31], 0, v[150:151]
	s_add_i32 m0, s34, 0x2000
	s_nop 0
	global_load_lds_dwordx4 v[128:129], off
	s_waitcnt vmcnt(6)
	s_barrier
	s_setprio 1
	v_mfma_f32_16x16x32_f16 v[52:55], v[204:207], v[158:161], v[52:55]
	v_mfma_f32_16x16x32_f16 v[44:47], v[212:215], v[158:161], v[44:47]
	v_mfma_f32_16x16x32_f16 v[36:39], v[204:207], v[180:183], v[36:39]
	v_mfma_f32_16x16x32_f16 v[28:31], v[212:215], v[180:183], v[28:31]
	v_mfma_f32_16x16x32_f16 v[20:23], v[204:207], v[188:191], v[20:23]
	v_mfma_f32_16x16x32_f16 v[12:15], v[212:215], v[188:191], v[12:15]
	v_mfma_f32_16x16x32_f16 v[4:7], v[204:207], v[196:199], v[4:7]
	v_mfma_f32_16x16x32_f16 v[0:3], v[212:215], v[196:199], v[0:3]
	v_mfma_f32_16x16x32_f16 v[52:55], v[208:211], v[176:179], v[52:55]
	v_mfma_f32_16x16x32_f16 v[44:47], v[216:219], v[176:179], v[44:47]
	v_mfma_f32_16x16x32_f16 v[36:39], v[208:211], v[184:187], v[36:39]
	v_mfma_f32_16x16x32_f16 v[28:31], v[216:219], v[184:187], v[28:31]
	v_mfma_f32_16x16x32_f16 v[20:23], v[208:211], v[192:195], v[20:23]
	v_mfma_f32_16x16x32_f16 v[12:15], v[216:219], v[192:195], v[12:15]
	v_mfma_f32_16x16x32_f16 v[4:7], v[208:211], v[200:203], v[4:7]
	v_mfma_f32_16x16x32_f16 v[0:3], v[216:219], v[200:203], v[0:3]
	s_setprio 0
	s_add_i32 s73, s73, 2
	s_add_u32 s28, s28, 0x100
	s_addc_u32 s29, s29, 0
	s_add_u32 s71, s71, 0x100
	s_addc_u32 s72, s72, 0
	s_cmp_gt_u32 s73, 9
	s_barrier
	s_cbranch_scc0 .LBB7_27
	s_lshl_b32 s28, s70, 8
	s_add_i32 s28, s28, s48
	s_lshl_b32 s29, s67, 8
	s_or_b32 s29, s29, s51
	v_add_u32_e32 v250, s28, v167
	v_mul_lo_u32 v250, v250, s10
	v_add_u32_e32 v250, s29, v250
	v_lshl_add_u32 v250, v250, 1, v168
	v_mov_b32_e32 v251, 0
	s_waitcnt vmcnt(6)
	v_pk_fma_f32 v[124:125], v[124:125], v[226:227], v[234:235] op_sel_hi:[1,0,1]
	v_pk_fma_f32 v[126:127], v[126:127], v[226:227], v[236:237] op_sel_hi:[1,0,1]
	v_pk_fma_f32 v[120:121], v[120:121], v[226:227], v[238:239] op_sel_hi:[1,0,1]
	v_pk_fma_f32 v[122:123], v[122:123], v[226:227], v[240:241] op_sel_hi:[1,0,1]
	v_cvt_pk_f16_f32 v124, v124, v125
	v_cvt_pk_f16_f32 v125, v126, v127
	v_cvt_pk_f16_f32 v126, v120, v121
	v_cvt_pk_f16_f32 v127, v122, v123
	ds_write_b128 v173, v[124:127]
	v_mov_b32_e32 v120, v251
	v_mov_b32_e32 v121, v251
	v_mov_b32_e32 v122, v251
	v_mov_b32_e32 v123, v251
	v_mov_b32_e32 v124, v251
	v_mov_b32_e32 v125, v251
	v_mov_b32_e32 v126, v251
	v_mov_b32_e32 v127, v251
	v_pk_fma_f32 v[116:117], v[116:117], v[226:227], v[242:243] op_sel_hi:[1,0,1]
	v_pk_fma_f32 v[118:119], v[118:119], v[226:227], v[244:245] op_sel_hi:[1,0,1]
	v_pk_fma_f32 v[112:113], v[112:113], v[226:227], v[246:247] op_sel_hi:[1,0,1]
	v_pk_fma_f32 v[114:115], v[114:115], v[226:227], v[248:249] op_sel_hi:[1,0,1]
	v_cvt_pk_f16_f32 v116, v116, v117
	v_cvt_pk_f16_f32 v117, v118, v119
	v_cvt_pk_f16_f32 v118, v112, v113
	v_cvt_pk_f16_f32 v119, v114, v115
	ds_write_b128 v173, v[116:119] offset:64
	v_mov_b32_e32 v112, v251
	v_mov_b32_e32 v113, v251
	v_mov_b32_e32 v114, v251
	v_mov_b32_e32 v115, v251
	v_mov_b32_e32 v116, v251
	v_mov_b32_e32 v117, v251
	v_mov_b32_e32 v118, v251
	v_mov_b32_e32 v119, v251
	ds_read_b128 v[176:179], v174
	ds_read_b128 v[180:183], v174 offset:1152
	v_pk_fma_f32 v[108:109], v[108:109], v[226:227], v[234:235] op_sel:[0,1,0]
	v_pk_fma_f32 v[110:111], v[110:111], v[226:227], v[236:237] op_sel:[0,1,0]
	v_pk_fma_f32 v[104:105], v[104:105], v[226:227], v[238:239] op_sel:[0,1,0]
	v_pk_fma_f32 v[106:107], v[106:107], v[226:227], v[240:241] op_sel:[0,1,0]
	v_cvt_pk_f16_f32 v108, v108, v109
	v_cvt_pk_f16_f32 v109, v110, v111
	v_cvt_pk_f16_f32 v110, v104, v105
	v_cvt_pk_f16_f32 v111, v106, v107
	s_waitcnt lgkmcnt(0)
	s_mul_i32 s34, s10, 0
	buffer_store_dwordx4 v[176:179], v250, s[20:23], s34 offen nt
	s_mul_i32 s35, s10, 16
	buffer_store_dwordx4 v[180:183], v250, s[20:23], s35 offen nt
	ds_write_b128 v173, v[108:111]
	v_mov_b32_e32 v104, v251
	v_mov_b32_e32 v105, v251
	v_mov_b32_e32 v106, v251
	v_mov_b32_e32 v107, v251
	v_mov_b32_e32 v108, v251
	v_mov_b32_e32 v109, v251
	v_mov_b32_e32 v110, v251
	v_mov_b32_e32 v111, v251
	v_pk_fma_f32 v[100:101], v[100:101], v[226:227], v[242:243] op_sel:[0,1,0]
	v_pk_fma_f32 v[102:103], v[102:103], v[226:227], v[244:245] op_sel:[0,1,0]
	v_pk_fma_f32 v[92:93], v[92:93], v[226:227], v[246:247] op_sel:[0,1,0]
	v_pk_fma_f32 v[94:95], v[94:95], v[226:227], v[248:249] op_sel:[0,1,0]
	v_cvt_pk_f16_f32 v100, v100, v101
	v_cvt_pk_f16_f32 v101, v102, v103
	v_cvt_pk_f16_f32 v102, v92, v93
	v_cvt_pk_f16_f32 v103, v94, v95
	ds_write_b128 v173, v[100:103] offset:64
	v_mov_b32_e32 v92, v251
	v_mov_b32_e32 v93, v251
	v_mov_b32_e32 v94, v251
	v_mov_b32_e32 v95, v251
	v_mov_b32_e32 v100, v251
	v_mov_b32_e32 v101, v251
	v_mov_b32_e32 v102, v251
	v_mov_b32_e32 v103, v251
	ds_read_b128 v[184:187], v174
	ds_read_b128 v[188:191], v174 offset:1152
	v_pk_fma_f32 v[96:97], v[96:97], v[228:229], v[234:235] op_sel_hi:[1,0,1]
	v_pk_fma_f32 v[98:99], v[98:99], v[228:229], v[236:237] op_sel_hi:[1,0,1]
	v_pk_fma_f32 v[88:89], v[88:89], v[228:229], v[238:239] op_sel_hi:[1,0,1]
	v_pk_fma_f32 v[90:91], v[90:91], v[228:229], v[240:241] op_sel_hi:[1,0,1]
	v_cvt_pk_f16_f32 v96, v96, v97
	v_cvt_pk_f16_f32 v97, v98, v99
	v_cvt_pk_f16_f32 v98, v88, v89
	v_cvt_pk_f16_f32 v99, v90, v91
	s_waitcnt lgkmcnt(0)
	s_mul_i32 s34, s10, 32
	buffer_store_dwordx4 v[184:187], v250, s[20:23], s34 offen nt
	s_mul_i32 s35, s10, 48
	buffer_store_dwordx4 v[188:191], v250, s[20:23], s35 offen nt
	ds_write_b128 v173, v[96:99]
	v_mov_b32_e32 v88, v251
	v_mov_b32_e32 v89, v251
	v_mov_b32_e32 v90, v251
	v_mov_b32_e32 v91, v251
	v_mov_b32_e32 v96, v251
	v_mov_b32_e32 v97, v251
	v_mov_b32_e32 v98, v251
	v_mov_b32_e32 v99, v251
	v_pk_fma_f32 v[84:85], v[84:85], v[228:229], v[242:243] op_sel_hi:[1,0,1]
	v_pk_fma_f32 v[86:87], v[86:87], v[228:229], v[244:245] op_sel_hi:[1,0,1]
	v_pk_fma_f32 v[76:77], v[76:77], v[228:229], v[246:247] op_sel_hi:[1,0,1]
	v_pk_fma_f32 v[78:79], v[78:79], v[228:229], v[248:249] op_sel_hi:[1,0,1]
	v_cvt_pk_f16_f32 v84, v84, v85
	v_cvt_pk_f16_f32 v85, v86, v87
	v_cvt_pk_f16_f32 v86, v76, v77
	v_cvt_pk_f16_f32 v87, v78, v79
	ds_write_b128 v173, v[84:87] offset:64
	v_mov_b32_e32 v76, v251
	v_mov_b32_e32 v77, v251
	v_mov_b32_e32 v78, v251
	v_mov_b32_e32 v79, v251
	v_mov_b32_e32 v84, v251
	v_mov_b32_e32 v85, v251
	v_mov_b32_e32 v86, v251
	v_mov_b32_e32 v87, v251
	ds_read_b128 v[176:179], v174
	ds_read_b128 v[180:183], v174 offset:1152
	v_pk_fma_f32 v[80:81], v[80:81], v[228:229], v[234:235] op_sel:[0,1,0]
	v_pk_fma_f32 v[82:83], v[82:83], v[228:229], v[236:237] op_sel:[0,1,0]
	v_pk_fma_f32 v[72:73], v[72:73], v[228:229], v[238:239] op_sel:[0,1,0]
	v_pk_fma_f32 v[74:75], v[74:75], v[228:229], v[240:241] op_sel:[0,1,0]
	v_cvt_pk_f16_f32 v80, v80, v81
	v_cvt_pk_f16_f32 v81, v82, v83
	v_cvt_pk_f16_f32 v82, v72, v73
	v_cvt_pk_f16_f32 v83, v74, v75
	s_waitcnt lgkmcnt(0)
	s_mul_i32 s34, s10, 64
	buffer_store_dwordx4 v[176:179], v250, s[20:23], s34 offen nt
	s_mul_i32 s35, s10, 80
	buffer_store_dwordx4 v[180:183], v250, s[20:23], s35 offen nt
	ds_write_b128 v173, v[80:83]
	v_mov_b32_e32 v72, v251
	v_mov_b32_e32 v73, v251
	v_mov_b32_e32 v74, v251
	v_mov_b32_e32 v75, v251
	v_mov_b32_e32 v80, v251
	v_mov_b32_e32 v81, v251
	v_mov_b32_e32 v82, v251
	v_mov_b32_e32 v83, v251
	v_pk_fma_f32 v[68:69], v[68:69], v[228:229], v[242:243] op_sel:[0,1,0]
	v_pk_fma_f32 v[70:71], v[70:71], v[228:229], v[244:245] op_sel:[0,1,0]
	v_pk_fma_f32 v[64:65], v[64:65], v[228:229], v[246:247] op_sel:[0,1,0]
	v_pk_fma_f32 v[66:67], v[66:67], v[228:229], v[248:249] op_sel:[0,1,0]
	v_cvt_pk_f16_f32 v68, v68, v69
	v_cvt_pk_f16_f32 v69, v70, v71
	v_cvt_pk_f16_f32 v70, v64, v65
	v_cvt_pk_f16_f32 v71, v66, v67
	ds_write_b128 v173, v[68:71] offset:64
	v_mov_b32_e32 v64, v251
	v_mov_b32_e32 v65, v251
	v_mov_b32_e32 v66, v251
	v_mov_b32_e32 v67, v251
	v_mov_b32_e32 v68, v251
	v_mov_b32_e32 v69, v251
	v_mov_b32_e32 v70, v251
	v_mov_b32_e32 v71, v251
	ds_read_b128 v[184:187], v174
	ds_read_b128 v[188:191], v174 offset:1152
	v_pk_fma_f32 v[60:61], v[60:61], v[230:231], v[234:235] op_sel_hi:[1,0,1]
	v_pk_fma_f32 v[62:63], v[62:63], v[230:231], v[236:237] op_sel_hi:[1,0,1]
	v_pk_fma_f32 v[56:57], v[56:57], v[230:231], v[238:239] op_sel_hi:[1,0,1]
	v_pk_fma_f32 v[58:59], v[58:59], v[230:231], v[240:241] op_sel_hi:[1,0,1]
	v_cvt_pk_f16_f32 v60, v60, v61
	v_cvt_pk_f16_f32 v61, v62, v63
	v_cvt_pk_f16_f32 v62, v56, v57
	v_cvt_pk_f16_f32 v63, v58, v59
	s_waitcnt lgkmcnt(0)
	s_mul_i32 s34, s10, 96
	buffer_store_dwordx4 v[184:187], v250, s[20:23], s34 offen nt
	s_mul_i32 s35, s10, 112
	buffer_store_dwordx4 v[188:191], v250, s[20:23], s35 offen nt
	ds_write_b128 v173, v[60:63]
	v_mov_b32_e32 v56, v251
	v_mov_b32_e32 v57, v251
	v_mov_b32_e32 v58, v251
	v_mov_b32_e32 v59, v251
	v_mov_b32_e32 v60, v251
	v_mov_b32_e32 v61, v251
	v_mov_b32_e32 v62, v251
	v_mov_b32_e32 v63, v251
	v_pk_fma_f32 v[52:53], v[52:53], v[230:231], v[242:243] op_sel_hi:[1,0,1]
	v_pk_fma_f32 v[54:55], v[54:55], v[230:231], v[244:245] op_sel_hi:[1,0,1]
	v_pk_fma_f32 v[44:45], v[44:45], v[230:231], v[246:247] op_sel_hi:[1,0,1]
	v_pk_fma_f32 v[46:47], v[46:47], v[230:231], v[248:249] op_sel_hi:[1,0,1]
	v_cvt_pk_f16_f32 v52, v52, v53
	v_cvt_pk_f16_f32 v53, v54, v55
	v_cvt_pk_f16_f32 v54, v44, v45
	v_cvt_pk_f16_f32 v55, v46, v47
	ds_write_b128 v173, v[52:55] offset:64
	v_mov_b32_e32 v44, v251
	v_mov_b32_e32 v45, v251
	v_mov_b32_e32 v46, v251
	v_mov_b32_e32 v47, v251
	v_mov_b32_e32 v52, v251
	v_mov_b32_e32 v53, v251
	v_mov_b32_e32 v54, v251
	v_mov_b32_e32 v55, v251
	ds_read_b128 v[176:179], v174
	ds_read_b128 v[180:183], v174 offset:1152
	v_pk_fma_f32 v[48:49], v[48:49], v[230:231], v[234:235] op_sel:[0,1,0]
	v_pk_fma_f32 v[50:51], v[50:51], v[230:231], v[236:237] op_sel:[0,1,0]
	v_pk_fma_f32 v[40:41], v[40:41], v[230:231], v[238:239] op_sel:[0,1,0]
	v_pk_fma_f32 v[42:43], v[42:43], v[230:231], v[240:241] op_sel:[0,1,0]
	v_cvt_pk_f16_f32 v48, v48, v49
	v_cvt_pk_f16_f32 v49, v50, v51
	v_cvt_pk_f16_f32 v50, v40, v41
	v_cvt_pk_f16_f32 v51, v42, v43
	s_waitcnt lgkmcnt(0)
	s_mul_i32 s34, s10, 256
	buffer_store_dwordx4 v[176:179], v250, s[20:23], s34 offen nt
	s_mul_i32 s35, s10, 272
	buffer_store_dwordx4 v[180:183], v250, s[20:23], s35 offen nt
	ds_write_b128 v173, v[48:51]
	v_mov_b32_e32 v40, v251
	v_mov_b32_e32 v41, v251
	v_mov_b32_e32 v42, v251
	v_mov_b32_e32 v43, v251
	v_mov_b32_e32 v48, v251
	v_mov_b32_e32 v49, v251
	v_mov_b32_e32 v50, v251
	v_mov_b32_e32 v51, v251
	v_pk_fma_f32 v[36:37], v[36:37], v[230:231], v[242:243] op_sel:[0,1,0]
	v_pk_fma_f32 v[38:39], v[38:39], v[230:231], v[244:245] op_sel:[0,1,0]
	v_pk_fma_f32 v[28:29], v[28:29], v[230:231], v[246:247] op_sel:[0,1,0]
	v_pk_fma_f32 v[30:31], v[30:31], v[230:231], v[248:249] op_sel:[0,1,0]
	v_cvt_pk_f16_f32 v36, v36, v37
	v_cvt_pk_f16_f32 v37, v38, v39
	v_cvt_pk_f16_f32 v38, v28, v29
	v_cvt_pk_f16_f32 v39, v30, v31
	ds_write_b128 v173, v[36:39] offset:64
	v_mov_b32_e32 v28, v251
	v_mov_b32_e32 v29, v251
	v_mov_b32_e32 v30, v251
	v_mov_b32_e32 v31, v251
	v_mov_b32_e32 v36, v251
	v_mov_b32_e32 v37, v251
	v_mov_b32_e32 v38, v251
	v_mov_b32_e32 v39, v251
	ds_read_b128 v[184:187], v174
	ds_read_b128 v[188:191], v174 offset:1152
	v_pk_fma_f32 v[32:33], v[32:33], v[232:233], v[234:235] op_sel_hi:[1,0,1]
	v_pk_fma_f32 v[34:35], v[34:35], v[232:233], v[236:237] op_sel_hi:[1,0,1]
	v_pk_fma_f32 v[24:25], v[24:25], v[232:233], v[238:239] op_sel_hi:[1,0,1]
	v_pk_fma_f32 v[26:27], v[26:27], v[232:233], v[240:241] op_sel_hi:[1,0,1]
	v_cvt_pk_f16_f32 v32, v32, v33
	v_cvt_pk_f16_f32 v33, v34, v35
	v_cvt_pk_f16_f32 v34, v24, v25
	v_cvt_pk_f16_f32 v35, v26, v27
	s_waitcnt lgkmcnt(0)
	s_mul_i32 s34, s10, 288
	buffer_store_dwordx4 v[184:187], v250, s[20:23], s34 offen nt
	s_mul_i32 s35, s10, 304
	buffer_store_dwordx4 v[188:191], v250, s[20:23], s35 offen nt
	ds_write_b128 v173, v[32:35]
	v_mov_b32_e32 v24, v251
	v_mov_b32_e32 v25, v251
	v_mov_b32_e32 v26, v251
	v_mov_b32_e32 v27, v251
	v_mov_b32_e32 v32, v251
	v_mov_b32_e32 v33, v251
	v_mov_b32_e32 v34, v251
	v_mov_b32_e32 v35, v251
	v_pk_fma_f32 v[20:21], v[20:21], v[232:233], v[242:243] op_sel_hi:[1,0,1]
	v_pk_fma_f32 v[22:23], v[22:23], v[232:233], v[244:245] op_sel_hi:[1,0,1]
	v_pk_fma_f32 v[12:13], v[12:13], v[232:233], v[246:247] op_sel_hi:[1,0,1]
	v_pk_fma_f32 v[14:15], v[14:15], v[232:233], v[248:249] op_sel_hi:[1,0,1]
	v_cvt_pk_f16_f32 v20, v20, v21
	v_cvt_pk_f16_f32 v21, v22, v23
	v_cvt_pk_f16_f32 v22, v12, v13
	v_cvt_pk_f16_f32 v23, v14, v15
	ds_write_b128 v173, v[20:23] offset:64
	v_mov_b32_e32 v12, v251
	v_mov_b32_e32 v13, v251
	v_mov_b32_e32 v14, v251
	v_mov_b32_e32 v15, v251
	v_mov_b32_e32 v20, v251
	v_mov_b32_e32 v21, v251
	v_mov_b32_e32 v22, v251
	v_mov_b32_e32 v23, v251
	ds_read_b128 v[176:179], v174
	ds_read_b128 v[180:183], v174 offset:1152
	v_pk_fma_f32 v[16:17], v[16:17], v[232:233], v[234:235] op_sel:[0,1,0]
	v_pk_fma_f32 v[18:19], v[18:19], v[232:233], v[236:237] op_sel:[0,1,0]
	v_pk_fma_f32 v[8:9], v[8:9], v[232:233], v[238:239] op_sel:[0,1,0]
	v_pk_fma_f32 v[10:11], v[10:11], v[232:233], v[240:241] op_sel:[0,1,0]
	v_cvt_pk_f16_f32 v16, v16, v17
	v_cvt_pk_f16_f32 v17, v18, v19
	v_cvt_pk_f16_f32 v18, v8, v9
	v_cvt_pk_f16_f32 v19, v10, v11
	s_waitcnt lgkmcnt(0)
	s_mul_i32 s34, s10, 320
	buffer_store_dwordx4 v[176:179], v250, s[20:23], s34 offen nt
	s_mul_i32 s35, s10, 336
	buffer_store_dwordx4 v[180:183], v250, s[20:23], s35 offen nt
	ds_write_b128 v173, v[16:19]
	v_mov_b32_e32 v8, v251
	v_mov_b32_e32 v9, v251
	v_mov_b32_e32 v10, v251
	v_mov_b32_e32 v11, v251
	v_mov_b32_e32 v16, v251
	v_mov_b32_e32 v17, v251
	v_mov_b32_e32 v18, v251
	v_mov_b32_e32 v19, v251
	v_pk_fma_f32 v[4:5], v[4:5], v[232:233], v[242:243] op_sel:[0,1,0]
	v_pk_fma_f32 v[6:7], v[6:7], v[232:233], v[244:245] op_sel:[0,1,0]
	v_pk_fma_f32 v[0:1], v[0:1], v[232:233], v[246:247] op_sel:[0,1,0]
	v_pk_fma_f32 v[2:3], v[2:3], v[232:233], v[248:249] op_sel:[0,1,0]
	v_cvt_pk_f16_f32 v4, v4, v5
	v_cvt_pk_f16_f32 v5, v6, v7
	v_cvt_pk_f16_f32 v6, v0, v1
	v_cvt_pk_f16_f32 v7, v2, v3
	ds_write_b128 v173, v[4:7] offset:64
	v_mov_b32_e32 v0, v251
	v_mov_b32_e32 v1, v251
	v_mov_b32_e32 v2, v251
	v_mov_b32_e32 v3, v251
	v_mov_b32_e32 v4, v251
	v_mov_b32_e32 v5, v251
	v_mov_b32_e32 v6, v251
	v_mov_b32_e32 v7, v251
	ds_read_b128 v[184:187], v174
	ds_read_b128 v[188:191], v174 offset:1152
	s_waitcnt lgkmcnt(0)
	s_mul_i32 s34, s10, 352
	buffer_store_dwordx4 v[184:187], v250, s[20:23], s34 offen nt
	s_mul_i32 s35, s10, 368
	buffer_store_dwordx4 v[188:191], v250, s[20:23], s35 offen nt
	s_mov_b32 s67, s68
	s_mov_b32 s70, s69
	s_mov_b64 s[30:31], s[0:1]
	s_mov_b64 s[28:29], s[8:9]
	s_mov_b64 vcc, s[6:7]
	s_cbranch_vccz .LBB7_12
	s_waitcnt vmcnt(0)
	s_cmpk_gt_u32 s36, 0xff
	s_cbranch_scc1 .LBB7_31
	s_barrier

.LBB7_32:
	s_endpgm
	s_endpgm
	s_endpgm
	s_endpgm
	s_endpgm
	s_endpgm
	s_endpgm
	s_endpgm
	s_endpgm
	s_endpgm
	s_endpgm
	s_endpgm
	s_endpgm
	s_endpgm
	s_endpgm
	s_endpgm
	s_endpgm
	s_endpgm
	s_endpgm
	s_endpgm
	s_endpgm
	s_endpgm
	s_endpgm
	s_endpgm
	s_endpgm
	s_endpgm
	s_endpgm
	s_endpgm
	s_endpgm
	s_endpgm
	s_endpgm
	s_endpgm
	s_endpgm
	s_endpgm
	s_endpgm
	s_endpgm
	s_endpgm
	s_endpgm
	s_endpgm
	s_endpgm
	s_endpgm
	s_endpgm
	s_endpgm
	s_endpgm
	s_endpgm
	s_endpgm
	s_endpgm
	s_endpgm
	s_endpgm
	s_endpgm
	s_endpgm
	s_endpgm
	s_endpgm
	s_endpgm
	s_endpgm
	s_endpgm
	s_endpgm
	s_endpgm
	s_endpgm

.LBB9_11:
	s_mov_b64 s[26:27], 0x80
	s_and_b32 s22, s20, 3
	s_add_i32 m0, s43, 0x18000
	v_lshl_add_u64 v[8:9], v[8:9], 0, s[26:27]
	s_lshl_b32 s48, s21, 6
	s_lshl_b32 s21, s21, 13
	s_lshl_b32 s23, s22, 12
	s_waitcnt vmcnt(4)
	s_barrier
	global_load_lds_dwordx4 v[8:9], off
	v_lshl_add_u64 v[6:7], v[6:7], 0, s[26:27]
	s_add_i32 m0, s43, 0x1a000
	s_add_i32 s49, s43, 0x8000
	s_add_i32 s50, s43, 0xa000
	global_load_lds_dwordx4 v[6:7], off
	v_lshl_add_u64 v[4:5], v[4:5], 0, s[26:27]
	s_mov_b32 m0, s49
	s_add_u32 s0, s30, 0xc080
	global_load_lds_dwordx4 v[4:5], off
	v_lshl_add_u64 v[2:3], v[2:3], 0, s[26:27]
	s_mov_b32 m0, s50
	s_addc_u32 s1, s31, 0
	global_load_lds_dwordx4 v[2:3], off
	s_add_i32 m0, s43, 0x1c000
	v_lshl_add_u64 v[2:3], s[0:1], 0, v[146:147]
	global_load_lds_dwordx4 v[2:3], off
	v_lshl_add_u64 v[2:3], s[0:1], 0, v[150:151]
	s_add_i32 m0, s43, 0x1e000
	s_lshl_b32 s53, s33, 2
	global_load_lds_dwordx4 v[2:3], off
	s_abs_i32 s54, s53
	v_cvt_f32_u32_e32 v6, s54
	v_and_b32_e32 v167, 15, v0
	v_and_b32_e32 v2, 48, v0
	v_lshlrev_b32_e32 v4, 2, v0
	v_rcp_iflag_f32_e32 v6, v6
	v_lshlrev_b32_e32 v5, 6, v0
	v_bfe_u32 v169, v0, 3, 3
	v_and_b32_e32 v0, 7, v0
	s_abs_i32 s57, s33
	v_lshlrev_b32_e32 v170, 4, v0
	v_add_lshl_u32 v171, v0, s10, 4
	v_mul_f32_e32 v0, 0x4f7ffffe, v6
	v_cvt_f32_u32_e32 v6, s57
	s_movk_i32 s0, 0x3c0
	s_mulk_i32 s20, 0x900
	v_cvt_u32_f32_e32 v0, v0
	v_rcp_iflag_f32_e32 v6, v6
	v_and_or_b32 v5, v5, s0, v2
	s_add_i32 s0, s20, 0
	v_lshl_or_b32 v3, v167, 6, v2
	v_and_b32_e32 v4, 32, v4
	s_add_i32 s0, s0, 0x20000
	v_bitop3_b32 v3, v3, s21, v4 bitop3:0xde
	v_bitop3_b32 v168, s23, v5, v4 bitop3:0xf6
	s_movk_i32 s1, 0x90
	v_mov_b32_e32 v4, s0
	v_mad_u32_u24 v5, v167, s1, v4
	v_mad_u32_u24 v4, v169, s1, v4
	v_readfirstlane_b32 s1, v0
	v_mul_f32_e32 v0, 0x4f7ffffe, v6
	v_cvt_u32_f32_e32 v0, v0
	s_sub_i32 s0, 0, s54
	s_mul_i32 s0, s0, s1
	s_mul_hi_u32 s0, s1, s0
	s_add_i32 s59, s1, s0
	s_sub_i32 s0, 0, s57
	v_readfirstlane_b32 s1, v0
	s_waitcnt vmcnt(6)
	s_mul_i32 s0, s0, s1
	v_add_u16_e32 v0, v1, v10
	s_mul_hi_u32 s0, s1, s0
	v_lshrrev_b16_e32 v0, 1, v0
	s_add_i32 s65, 0, 0x10000
	s_add_i32 s66, 0, 0x14000
	s_mov_b32 s23, 0x20000
	s_lshl_b32 s51, s22, 6
	s_waitcnt lgkmcnt(0)
	s_ashr_i32 s52, s11, 31
	s_lshl_b32 s22, s10, 17
	s_and_b32 s21, s9, 0xffff
	s_mov_b32 s20, s8
	s_lshl_b32 s55, s10, 5
	s_mul_i32 s56, s10, 48
	s_bfe_i32 s58, s33, 0x1001c
	s_ashr_i32 s60, s33, 31
	s_add_i32 s61, s1, s0
	s_mul_i32 s62, s10, 0xc0
	s_mul_i32 s63, s10, 0x60
	s_lshl_b32 s64, s10, 4
	v_add_lshl_u32 v152, v11, v0, 1
	v_mov_b32_e32 v153, v147
	v_add_lshl_u32 v154, v12, v0, 1
	v_mov_b32_e32 v155, v147
	v_mov_b64_e32 v[156:157], s[6:7]
	v_add_u32_e32 v172, s65, v168
	v_add_u32_e32 v173, 0, v3
	v_add_u32_e32 v174, s66, v168
	v_add_u32_e32 v175, v5, v2
	v_add_u32_e32 v176, v4, v170
	s_barrier
	v_mov_b32_e32 v0, 0
	v_mov_b32_e32 v1, v0
	v_mov_b32_e32 v2, v0
	v_mov_b32_e32 v3, v0
	v_mov_b32_e32 v4, v0
	v_mov_b32_e32 v5, v0
	v_mov_b32_e32 v6, v0
	v_mov_b32_e32 v7, v0
	v_mov_b32_e32 v8, v0
	v_mov_b32_e32 v9, v0
	v_mov_b32_e32 v10, v0
	v_mov_b32_e32 v11, v0
	v_mov_b32_e32 v12, v0
	v_mov_b32_e32 v13, v0
	v_mov_b32_e32 v14, v0
	v_mov_b32_e32 v15, v0
	v_mov_b32_e32 v16, v0
	v_mov_b32_e32 v17, v0
	v_mov_b32_e32 v18, v0
	v_mov_b32_e32 v19, v0
	v_mov_b32_e32 v20, v0
	v_mov_b32_e32 v21, v0
	v_mov_b32_e32 v22, v0
	v_mov_b32_e32 v23, v0
	v_mov_b32_e32 v24, v0
	v_mov_b32_e32 v25, v0
	v_mov_b32_e32 v26, v0
	v_mov_b32_e32 v27, v0
	v_mov_b32_e32 v28, v0
	v_mov_b32_e32 v29, v0
	v_mov_b32_e32 v30, v0
	v_mov_b32_e32 v31, v0
	v_mov_b32_e32 v32, v0
	v_mov_b32_e32 v33, v0
	v_mov_b32_e32 v34, v0
	v_mov_b32_e32 v35, v0
	v_mov_b32_e32 v36, v0
	v_mov_b32_e32 v37, v0
	v_mov_b32_e32 v38, v0
	v_mov_b32_e32 v39, v0
	v_mov_b32_e32 v40, v0
	v_mov_b32_e32 v41, v0
	v_mov_b32_e32 v42, v0
	v_mov_b32_e32 v43, v0
	v_mov_b32_e32 v44, v0
	v_mov_b32_e32 v45, v0
	v_mov_b32_e32 v46, v0
	v_mov_b32_e32 v47, v0
	v_mov_b32_e32 v48, v0
	v_mov_b32_e32 v49, v0
	v_mov_b32_e32 v50, v0
	v_mov_b32_e32 v51, v0
	v_mov_b32_e32 v52, v0
	v_mov_b32_e32 v53, v0
	v_mov_b32_e32 v54, v0
	v_mov_b32_e32 v55, v0
	v_mov_b32_e32 v56, v0
	v_mov_b32_e32 v57, v0
	v_mov_b32_e32 v58, v0
	v_mov_b32_e32 v59, v0
	v_mov_b32_e32 v60, v0
	v_mov_b32_e32 v61, v0
	v_mov_b32_e32 v62, v0
	v_mov_b32_e32 v63, v0
	v_mov_b32_e32 v64, v0
	v_mov_b32_e32 v65, v0
	v_mov_b32_e32 v66, v0
	v_mov_b32_e32 v67, v0
	v_mov_b32_e32 v68, v0
	v_mov_b32_e32 v69, v0
	v_mov_b32_e32 v70, v0
	v_mov_b32_e32 v71, v0
	v_mov_b32_e32 v72, v0
	v_mov_b32_e32 v73, v0
	v_mov_b32_e32 v74, v0
	v_mov_b32_e32 v75, v0
	v_mov_b32_e32 v76, v0
	v_mov_b32_e32 v77, v0
	v_mov_b32_e32 v78, v0
	v_mov_b32_e32 v79, v0
	v_mov_b32_e32 v80, v0
	v_mov_b32_e32 v81, v0
	v_mov_b32_e32 v82, v0
	v_mov_b32_e32 v83, v0
	v_mov_b32_e32 v84, v0
	v_mov_b32_e32 v85, v0
	v_mov_b32_e32 v86, v0
	v_mov_b32_e32 v87, v0
	v_mov_b32_e32 v88, v0
	v_mov_b32_e32 v89, v0
	v_mov_b32_e32 v90, v0
	v_mov_b32_e32 v91, v0
	v_mov_b32_e32 v92, v0
	v_mov_b32_e32 v93, v0
	v_mov_b32_e32 v94, v0
	v_mov_b32_e32 v95, v0
	v_mov_b32_e32 v96, v0
	v_mov_b32_e32 v97, v0
	v_mov_b32_e32 v98, v0
	v_mov_b32_e32 v99, v0
	v_mov_b32_e32 v100, v0
	v_mov_b32_e32 v101, v0
	v_mov_b32_e32 v102, v0
	v_mov_b32_e32 v103, v0
	v_mov_b32_e32 v104, v0
	v_mov_b32_e32 v105, v0
	v_mov_b32_e32 v106, v0
	v_mov_b32_e32 v107, v0
	v_mov_b32_e32 v108, v0
	v_mov_b32_e32 v109, v0
	v_mov_b32_e32 v110, v0
	v_mov_b32_e32 v111, v0
	v_mov_b32_e32 v112, v0
	v_mov_b32_e32 v113, v0
	v_mov_b32_e32 v114, v0
	v_mov_b32_e32 v115, v0
	v_mov_b32_e32 v116, v0
	v_mov_b32_e32 v117, v0
	v_mov_b32_e32 v118, v0
	v_mov_b32_e32 v119, v0
	v_mov_b32_e32 v120, v0
	v_mov_b32_e32 v121, v0
	v_mov_b32_e32 v122, v0
	v_mov_b32_e32 v123, v0
	v_mov_b32_e32 v124, v0
	v_mov_b32_e32 v125, v0
	v_mov_b32_e32 v126, v0
	v_mov_b32_e32 v127, v0

.LBB9_26:
	s_lshl_b32 s34, s70, 8
	s_add_i32 s34, s34, s48
	v_or_b32_e32 v250, s34, v167
	v_ashrrev_i32_e32 v251, 31, v250
	v_lshl_add_u64 v[250:251], v[250:251], 3, s[12:13]
	s_lshl_b32 s35, s68, 8
	s_or_b32 s35, s35, s51
	v_or_b32_e32 v252, s35, v166
	v_ashrrev_i32_e32 v253, 31, v252
	v_lshl_add_u64 v[252:253], v[252:253], 2, s[14:15]
	global_load_dword v226, v[250:251], off offset:4
	global_load_dword v227, v[250:251], off offset:132
	global_load_dword v228, v[250:251], off offset:260
	global_load_dword v229, v[250:251], off offset:388
	global_load_dword v230, v[250:251], off offset:1028
	global_load_dword v231, v[250:251], off offset:1156
	global_load_dword v232, v[250:251], off offset:1284
	global_load_dword v233, v[250:251], off offset:1412
	global_load_dwordx4 v[234:237], v[252:253], off
	global_load_dwordx4 v[238:241], v[252:253], off offset:16
	global_load_dwordx4 v[242:245], v[252:253], off offset:128
	global_load_dwordx4 v[246:249], v[252:253], off offset:144
	s_add_u32 s28, s28, 0x30080
	s_addc_u32 s29, s29, 0
	s_add_u32 s71, s30, 0x100
	v_mov_b32_e32 v0, 0
	s_addc_u32 s72, s31, 0
	s_mov_b32 s73, -2
.LBB9_27:
	ds_read_b128 v[128:131], v172
	ds_read_b128 v[132:135], v172 offset:1024
	ds_read_b128 v[136:139], v172 offset:2048
	ds_read_b128 v[140:143], v172 offset:3072
	s_add_u32 s30, s28, 0xfffd0080
	s_addc_u32 s31, s29, -1
	s_cmp_eq_u32 s73, 8
	s_cselect_b32 s35, s9, s31
	s_cselect_b32 s34, s8, s30
	s_cselect_b32 s31, s1, s72
	s_cselect_b32 s30, s0, s71
	v_lshl_add_u64 v[202:203], s[28:29], 0, v[152:153]
	s_add_i32 m0, s43, 0xc000
	ds_read_b128 v[158:161], v173
	ds_read_b128 v[162:165], v173 offset:1024
	ds_read_b128 v[178:181], v173 offset:2048
	ds_read_b128 v[182:185], v173 offset:3072
	ds_read_b128 v[186:189], v173 offset:4096
	ds_read_b128 v[190:193], v173 offset:5120
	ds_read_b128 v[194:197], v173 offset:6144
	ds_read_b128 v[198:201], v173 offset:7168
	global_load_lds_dwordx4 v[202:203], off
	v_lshl_add_u64 v[202:203], s[28:29], 0, v[154:155]
	s_add_i32 m0, s43, 0xe000
	s_nop 0
	global_load_lds_dwordx4 v[202:203], off
	s_waitcnt lgkmcnt(8)
	s_barrier
	s_waitcnt lgkmcnt(0)
	s_setprio 1
	s_waitcnt lgkmcnt(0)
	v_mfma_f32_16x16x32_f16 v[124:127], v[128:131], v[158:161], v[124:127]
	v_mfma_f32_16x16x32_f16 v[120:123], v[136:139], v[158:161], v[120:123]
	v_mfma_f32_16x16x32_f16 v[108:111], v[128:131], v[178:181], v[108:111]
	v_mfma_f32_16x16x32_f16 v[104:107], v[136:139], v[178:181], v[104:107]
	v_mfma_f32_16x16x32_f16 v[96:99], v[128:131], v[186:189], v[96:99]
	v_mfma_f32_16x16x32_f16 v[88:91], v[136:139], v[186:189], v[88:91]
	v_mfma_f32_16x16x32_f16 v[80:83], v[128:131], v[194:197], v[80:83]
	v_mfma_f32_16x16x32_f16 v[72:75], v[136:139], v[194:197], v[72:75]
	v_mfma_f32_16x16x32_f16 v[124:127], v[132:135], v[162:165], v[124:127]
	v_mfma_f32_16x16x32_f16 v[120:123], v[140:143], v[162:165], v[120:123]
	v_mfma_f32_16x16x32_f16 v[108:111], v[132:135], v[182:185], v[108:111]
	v_mfma_f32_16x16x32_f16 v[104:107], v[140:143], v[182:185], v[104:107]
	v_mfma_f32_16x16x32_f16 v[96:99], v[132:135], v[190:193], v[96:99]
	v_mfma_f32_16x16x32_f16 v[88:91], v[140:143], v[190:193], v[88:91]
	v_mfma_f32_16x16x32_f16 v[80:83], v[132:135], v[198:201], v[80:83]
	v_mfma_f32_16x16x32_f16 v[72:75], v[140:143], v[198:201], v[72:75]
	s_setprio 0
	s_barrier
	s_add_i32 s74, s65, s42
	v_lshl_add_u64 v[218:219], s[30:31], 0, v[146:147]
	s_mov_b32 m0, s74
	ds_read_b128 v[202:205], v174
	ds_read_b128 v[206:209], v174 offset:1024
	ds_read_b128 v[210:213], v174 offset:2048
	ds_read_b128 v[214:217], v174 offset:3072
	global_load_lds_dwordx4 v[218:219], off
	v_lshl_add_u64 v[220:221], s[30:31], 0, v[150:151]
	s_add_i32 m0, s74, 0x2000
	s_nop 0
	global_load_lds_dwordx4 v[220:221], off
	s_barrier
	s_waitcnt lgkmcnt(0)
	s_setprio 1
	s_waitcnt lgkmcnt(0)
	v_mfma_f32_16x16x32_f16 v[116:119], v[202:205], v[158:161], v[116:119]
	v_mfma_f32_16x16x32_f16 v[112:115], v[210:213], v[158:161], v[112:115]
	v_mfma_f32_16x16x32_f16 v[100:103], v[202:205], v[178:181], v[100:103]
	v_mfma_f32_16x16x32_f16 v[92:95], v[210:213], v[178:181], v[92:95]
	v_mfma_f32_16x16x32_f16 v[84:87], v[202:205], v[186:189], v[84:87]
	v_mfma_f32_16x16x32_f16 v[76:79], v[210:213], v[186:189], v[76:79]
	v_mfma_f32_16x16x32_f16 v[68:71], v[202:205], v[194:197], v[68:71]
	v_mfma_f32_16x16x32_f16 v[64:67], v[210:213], v[194:197], v[64:67]
	v_mfma_f32_16x16x32_f16 v[116:119], v[206:209], v[162:165], v[116:119]
	v_mfma_f32_16x16x32_f16 v[112:115], v[214:217], v[162:165], v[112:115]
	v_mfma_f32_16x16x32_f16 v[100:103], v[206:209], v[182:185], v[100:103]
	v_mfma_f32_16x16x32_f16 v[92:95], v[214:217], v[182:185], v[92:95]
	v_mfma_f32_16x16x32_f16 v[84:87], v[206:209], v[190:193], v[84:87]
	v_mfma_f32_16x16x32_f16 v[76:79], v[214:217], v[190:193], v[76:79]
	v_mfma_f32_16x16x32_f16 v[68:71], v[206:209], v[198:201], v[68:71]
	v_mfma_f32_16x16x32_f16 v[64:67], v[214:217], v[198:201], v[64:67]
	s_setprio 0
	s_mov_b32 m0, s43
	v_lshl_add_u64 v[222:223], s[34:35], 0, v[144:145]
	s_barrier
	ds_read_b128 v[158:161], v173 offset:16384
	ds_read_b128 v[162:165], v173 offset:17408
	ds_read_b128 v[178:181], v173 offset:18432
	ds_read_b128 v[182:185], v173 offset:19456
	ds_read_b128 v[186:189], v173 offset:20480
	ds_read_b128 v[190:193], v173 offset:21504
	ds_read_b128 v[194:197], v173 offset:22528
	ds_read_b128 v[198:201], v173 offset:23552
	global_load_lds_dwordx4 v[222:223], off
	v_lshl_add_u64 v[224:225], s[34:35], 0, v[148:149]
	s_mov_b32 m0, s44
	s_nop 0
	global_load_lds_dwordx4 v[224:225], off
	s_barrier
	s_waitcnt lgkmcnt(0)
	s_setprio 1
	s_waitcnt lgkmcnt(0)
	v_mfma_f32_16x16x32_f16 v[60:63], v[128:131], v[158:161], v[60:63]
	v_mfma_f32_16x16x32_f16 v[56:59], v[136:139], v[158:161], v[56:59]
	v_mfma_f32_16x16x32_f16 v[48:51], v[128:131], v[178:181], v[48:51]
	v_mfma_f32_16x16x32_f16 v[40:43], v[136:139], v[178:181], v[40:43]
	v_mfma_f32_16x16x32_f16 v[32:35], v[128:131], v[186:189], v[32:35]
	v_mfma_f32_16x16x32_f16 v[24:27], v[136:139], v[186:189], v[24:27]
	v_mfma_f32_16x16x32_f16 v[16:19], v[128:131], v[194:197], v[16:19]
	v_mfma_f32_16x16x32_f16 v[8:11], v[136:139], v[194:197], v[8:11]
	v_mfma_f32_16x16x32_f16 v[60:63], v[132:135], v[162:165], v[60:63]
	v_mfma_f32_16x16x32_f16 v[56:59], v[140:143], v[162:165], v[56:59]
	v_mfma_f32_16x16x32_f16 v[48:51], v[132:135], v[182:185], v[48:51]
	v_mfma_f32_16x16x32_f16 v[40:43], v[140:143], v[182:185], v[40:43]
	v_mfma_f32_16x16x32_f16 v[32:35], v[132:135], v[190:193], v[32:35]
	v_mfma_f32_16x16x32_f16 v[24:27], v[140:143], v[190:193], v[24:27]
	v_mfma_f32_16x16x32_f16 v[16:19], v[132:135], v[198:201], v[16:19]
	v_mfma_f32_16x16x32_f16 v[8:11], v[140:143], v[198:201], v[8:11]
	s_setprio 0
	s_barrier
	s_add_u32 s74, s30, 0xc000
	s_addc_u32 s75, s31, 0
	s_add_i32 s76, s66, s42
	v_lshl_add_u64 v[128:129], s[74:75], 0, v[146:147]
	s_mov_b32 m0, s76
	s_nop 0
	global_load_lds_dwordx4 v[128:129], off
	v_lshl_add_u64 v[128:129], s[74:75], 0, v[150:151]
	s_add_i32 m0, s76, 0x2000
	s_nop 0
	global_load_lds_dwordx4 v[128:129], off
	s_waitcnt vmcnt(6)
	s_barrier
	s_setprio 1
	v_mfma_f32_16x16x32_f16 v[52:55], v[202:205], v[158:161], v[52:55]
	v_mfma_f32_16x16x32_f16 v[44:47], v[210:213], v[158:161], v[44:47]
	v_mfma_f32_16x16x32_f16 v[36:39], v[202:205], v[178:181], v[36:39]
	v_mfma_f32_16x16x32_f16 v[28:31], v[210:213], v[178:181], v[28:31]
	v_mfma_f32_16x16x32_f16 v[20:23], v[202:205], v[186:189], v[20:23]
	v_mfma_f32_16x16x32_f16 v[12:15], v[210:213], v[186:189], v[12:15]
	v_mfma_f32_16x16x32_f16 v[4:7], v[202:205], v[194:197], v[4:7]
	v_mfma_f32_16x16x32_f16 v[0:3], v[210:213], v[194:197], v[0:3]
	v_mfma_f32_16x16x32_f16 v[52:55], v[206:209], v[162:165], v[52:55]
	v_mfma_f32_16x16x32_f16 v[44:47], v[214:217], v[162:165], v[44:47]
	v_mfma_f32_16x16x32_f16 v[36:39], v[206:209], v[182:185], v[36:39]
	v_mfma_f32_16x16x32_f16 v[28:31], v[214:217], v[182:185], v[28:31]
	v_mfma_f32_16x16x32_f16 v[20:23], v[206:209], v[190:193], v[20:23]
	v_mfma_f32_16x16x32_f16 v[12:15], v[214:217], v[190:193], v[12:15]
	v_mfma_f32_16x16x32_f16 v[4:7], v[206:209], v[198:201], v[4:7]
	v_mfma_f32_16x16x32_f16 v[0:3], v[214:217], v[198:201], v[0:3]
	s_setprio 0
	s_add_i32 s74, 0, 0x18000
	v_add_u32_e32 v140, s74, v168
	s_barrier
	ds_read_b128 v[128:131], v140
	ds_read_b128 v[132:135], v140 offset:1024
	ds_read_b128 v[136:139], v140 offset:2048
	ds_read_b128 v[140:143], v140 offset:3072
	s_add_u32 s34, s34, 0x30000
	s_addc_u32 s35, s35, 0
	s_mov_b32 m0, s45
	v_lshl_add_u64 v[202:203], s[34:35], 0, v[144:145]
	ds_read_b128 v[158:161], v173 offset:32768
	ds_read_b128 v[162:165], v173 offset:33792
	ds_read_b128 v[178:181], v173 offset:34816
	ds_read_b128 v[182:185], v173 offset:35840
	ds_read_b128 v[186:189], v173 offset:36864
	ds_read_b128 v[190:193], v173 offset:37888
	ds_read_b128 v[194:197], v173 offset:38912
	ds_read_b128 v[198:201], v173 offset:39936
	global_load_lds_dwordx4 v[202:203], off
	v_lshl_add_u64 v[202:203], s[34:35], 0, v[148:149]
	s_mov_b32 m0, s46
	s_nop 0
	global_load_lds_dwordx4 v[202:203], off
	s_waitcnt lgkmcnt(8)
	s_barrier
	s_waitcnt lgkmcnt(0)
	s_setprio 1
	s_waitcnt lgkmcnt(0)
	v_mfma_f32_16x16x32_f16 v[124:127], v[128:131], v[158:161], v[124:127]
	v_mfma_f32_16x16x32_f16 v[120:123], v[136:139], v[158:161], v[120:123]
	v_mfma_f32_16x16x32_f16 v[108:111], v[128:131], v[178:181], v[108:111]
	v_mfma_f32_16x16x32_f16 v[104:107], v[136:139], v[178:181], v[104:107]
	v_mfma_f32_16x16x32_f16 v[96:99], v[128:131], v[186:189], v[96:99]
	v_mfma_f32_16x16x32_f16 v[88:91], v[136:139], v[186:189], v[88:91]
	v_mfma_f32_16x16x32_f16 v[80:83], v[128:131], v[194:197], v[80:83]
	v_mfma_f32_16x16x32_f16 v[72:75], v[136:139], v[194:197], v[72:75]
	v_mfma_f32_16x16x32_f16 v[124:127], v[132:135], v[162:165], v[124:127]
	v_mfma_f32_16x16x32_f16 v[120:123], v[140:143], v[162:165], v[120:123]
	v_mfma_f32_16x16x32_f16 v[108:111], v[132:135], v[182:185], v[108:111]
	v_mfma_f32_16x16x32_f16 v[104:107], v[140:143], v[182:185], v[104:107]
	v_mfma_f32_16x16x32_f16 v[96:99], v[132:135], v[190:193], v[96:99]
	v_mfma_f32_16x16x32_f16 v[88:91], v[140:143], v[190:193], v[88:91]
	v_mfma_f32_16x16x32_f16 v[80:83], v[132:135], v[198:201], v[80:83]
	v_mfma_f32_16x16x32_f16 v[72:75], v[140:143], v[198:201], v[72:75]
	s_setprio 0
	s_barrier
	s_add_i32 s34, 0, 0x1c000
	s_add_i32 s35, s74, s42
	v_add_u32_e32 v177, s34, v168
	v_lshl_add_u64 v[218:219], v[218:219], 0, s[26:27]
	s_mov_b32 m0, s35
	ds_read_b128 v[202:205], v177
	ds_read_b128 v[206:209], v177 offset:1024
	ds_read_b128 v[210:213], v177 offset:2048
	ds_read_b128 v[214:217], v177 offset:3072
	global_load_lds_dwordx4 v[218:219], off
	v_lshl_add_u64 v[218:219], v[220:221], 0, s[26:27]
	s_add_i32 m0, s35, 0x2000
	s_nop 0
	global_load_lds_dwordx4 v[218:219], off
	s_barrier
	s_waitcnt lgkmcnt(0)
	s_setprio 1
	s_waitcnt lgkmcnt(0)
	v_mfma_f32_16x16x32_f16 v[116:119], v[202:205], v[158:161], v[116:119]
	v_mfma_f32_16x16x32_f16 v[112:115], v[210:213], v[158:161], v[112:115]
	v_mfma_f32_16x16x32_f16 v[100:103], v[202:205], v[178:181], v[100:103]
	v_mfma_f32_16x16x32_f16 v[92:95], v[210:213], v[178:181], v[92:95]
	v_mfma_f32_16x16x32_f16 v[84:87], v[202:205], v[186:189], v[84:87]
	v_mfma_f32_16x16x32_f16 v[76:79], v[210:213], v[186:189], v[76:79]
	v_mfma_f32_16x16x32_f16 v[68:71], v[202:205], v[194:197], v[68:71]
	v_mfma_f32_16x16x32_f16 v[64:67], v[210:213], v[194:197], v[64:67]
	v_mfma_f32_16x16x32_f16 v[116:119], v[206:209], v[162:165], v[116:119]
	v_mfma_f32_16x16x32_f16 v[112:115], v[214:217], v[162:165], v[112:115]
	v_mfma_f32_16x16x32_f16 v[100:103], v[206:209], v[182:185], v[100:103]
	v_mfma_f32_16x16x32_f16 v[92:95], v[214:217], v[182:185], v[92:95]
	v_mfma_f32_16x16x32_f16 v[84:87], v[206:209], v[190:193], v[84:87]
	v_mfma_f32_16x16x32_f16 v[76:79], v[214:217], v[190:193], v[76:79]
	v_mfma_f32_16x16x32_f16 v[68:71], v[206:209], v[198:201], v[68:71]
	v_mfma_f32_16x16x32_f16 v[64:67], v[214:217], v[198:201], v[64:67]
	s_setprio 0
	s_mov_b32 m0, s49
	v_lshl_add_u64 v[218:219], v[222:223], 0, s[26:27]
	s_barrier
	ds_read_b128 v[158:161], v173 offset:49152
	ds_read_b128 v[162:165], v173 offset:50176
	ds_read_b128 v[178:181], v173 offset:51200
	ds_read_b128 v[182:185], v173 offset:52224
	ds_read_b128 v[186:189], v173 offset:53248
	ds_read_b128 v[190:193], v173 offset:54272
	ds_read_b128 v[194:197], v173 offset:55296
	ds_read_b128 v[198:201], v173 offset:56320
	global_load_lds_dwordx4 v[218:219], off
	v_lshl_add_u64 v[218:219], v[224:225], 0, s[26:27]
	s_mov_b32 m0, s50
	s_nop 0
	global_load_lds_dwordx4 v[218:219], off
	s_barrier
	s_waitcnt lgkmcnt(0)
	s_setprio 1
	s_waitcnt lgkmcnt(0)
	v_mfma_f32_16x16x32_f16 v[60:63], v[128:131], v[158:161], v[60:63]
	v_mfma_f32_16x16x32_f16 v[56:59], v[136:139], v[158:161], v[56:59]
	v_mfma_f32_16x16x32_f16 v[48:51], v[128:131], v[178:181], v[48:51]
	v_mfma_f32_16x16x32_f16 v[40:43], v[136:139], v[178:181], v[40:43]
	v_mfma_f32_16x16x32_f16 v[32:35], v[128:131], v[186:189], v[32:35]
	v_mfma_f32_16x16x32_f16 v[24:27], v[136:139], v[186:189], v[24:27]
	v_mfma_f32_16x16x32_f16 v[16:19], v[128:131], v[194:197], v[16:19]
	v_mfma_f32_16x16x32_f16 v[8:11], v[136:139], v[194:197], v[8:11]
	v_mfma_f32_16x16x32_f16 v[60:63], v[132:135], v[162:165], v[60:63]
	v_mfma_f32_16x16x32_f16 v[56:59], v[140:143], v[162:165], v[56:59]
	v_mfma_f32_16x16x32_f16 v[48:51], v[132:135], v[182:185], v[48:51]
	v_mfma_f32_16x16x32_f16 v[40:43], v[140:143], v[182:185], v[40:43]
	v_mfma_f32_16x16x32_f16 v[32:35], v[132:135], v[190:193], v[32:35]
	v_mfma_f32_16x16x32_f16 v[24:27], v[140:143], v[190:193], v[24:27]
	v_mfma_f32_16x16x32_f16 v[16:19], v[132:135], v[198:201], v[16:19]
	v_mfma_f32_16x16x32_f16 v[8:11], v[140:143], v[198:201], v[8:11]
	s_setprio 0
	s_barrier
	s_add_u32 s30, s30, 0xc080
	s_addc_u32 s31, s31, 0
	s_add_i32 s34, s34, s42
	v_lshl_add_u64 v[128:129], s[30:31], 0, v[146:147]
	s_mov_b32 m0, s34
	s_nop 0
	global_load_lds_dwordx4 v[128:129], off
	v_lshl_add_u64 v[128:129], s[30:31], 0, v[150:151]
	s_add_i32 m0, s34, 0x2000
	s_nop 0
	global_load_lds_dwordx4 v[128:129], off
	s_waitcnt vmcnt(6)
	s_barrier
	s_setprio 1
	v_mfma_f32_16x16x32_f16 v[52:55], v[202:205], v[158:161], v[52:55]
	v_mfma_f32_16x16x32_f16 v[44:47], v[210:213], v[158:161], v[44:47]
	v_mfma_f32_16x16x32_f16 v[36:39], v[202:205], v[178:181], v[36:39]
	v_mfma_f32_16x16x32_f16 v[28:31], v[210:213], v[178:181], v[28:31]
	v_mfma_f32_16x16x32_f16 v[20:23], v[202:205], v[186:189], v[20:23]
	v_mfma_f32_16x16x32_f16 v[12:15], v[210:213], v[186:189], v[12:15]
	v_mfma_f32_16x16x32_f16 v[4:7], v[202:205], v[194:197], v[4:7]
	v_mfma_f32_16x16x32_f16 v[0:3], v[210:213], v[194:197], v[0:3]
	v_mfma_f32_16x16x32_f16 v[52:55], v[206:209], v[162:165], v[52:55]
	v_mfma_f32_16x16x32_f16 v[44:47], v[214:217], v[162:165], v[44:47]
	v_mfma_f32_16x16x32_f16 v[36:39], v[206:209], v[182:185], v[36:39]
	v_mfma_f32_16x16x32_f16 v[28:31], v[214:217], v[182:185], v[28:31]
	v_mfma_f32_16x16x32_f16 v[20:23], v[206:209], v[190:193], v[20:23]
	v_mfma_f32_16x16x32_f16 v[12:15], v[214:217], v[190:193], v[12:15]
	v_mfma_f32_16x16x32_f16 v[4:7], v[206:209], v[198:201], v[4:7]
	v_mfma_f32_16x16x32_f16 v[0:3], v[214:217], v[198:201], v[0:3]
	s_setprio 0
	s_add_i32 s73, s73, 2
	s_add_u32 s28, s28, 0x100
	s_addc_u32 s29, s29, 0
	s_add_u32 s71, s71, 0x100
	s_addc_u32 s72, s72, 0
	s_cmp_gt_u32 s73, 9
	s_barrier
	s_cbranch_scc0 .LBB9_27
	s_lshl_b32 s28, s70, 8
	s_add_i32 s28, s28, s48
	s_lshl_b32 s29, s68, 8
	s_or_b32 s29, s29, s51
	v_add_u32_e32 v250, s28, v169
	v_mul_lo_u32 v250, v250, s10
	v_add_u32_e32 v250, s29, v250
	v_lshl_add_u32 v250, v250, 1, v170
	v_mov_b32_e32 v251, 0
	s_waitcnt vmcnt(6)
	v_pk_fma_f32 v[124:125], v[124:125], v[226:227], v[234:235] op_sel_hi:[1,0,1]
	v_pk_fma_f32 v[126:127], v[126:127], v[226:227], v[236:237] op_sel_hi:[1,0,1]
	v_pk_fma_f32 v[120:121], v[120:121], v[226:227], v[238:239] op_sel_hi:[1,0,1]
	v_pk_fma_f32 v[122:123], v[122:123], v[226:227], v[240:241] op_sel_hi:[1,0,1]
	v_cvt_pk_f16_f32 v124, v124, v125
	v_cvt_pk_f16_f32 v125, v126, v127
	v_cvt_pk_f16_f32 v126, v120, v121
	v_cvt_pk_f16_f32 v127, v122, v123
	v_pk_max_f16 v124, v124, 0
	v_pk_max_f16 v125, v125, 0
	v_pk_max_f16 v126, v126, 0
	v_pk_max_f16 v127, v127, 0
	ds_write_b128 v175, v[124:127]
	v_mov_b32_e32 v120, v251
	v_mov_b32_e32 v121, v251
	v_mov_b32_e32 v122, v251
	v_mov_b32_e32 v123, v251
	v_mov_b32_e32 v124, v251
	v_mov_b32_e32 v125, v251
	v_mov_b32_e32 v126, v251
	v_mov_b32_e32 v127, v251
	v_pk_fma_f32 v[116:117], v[116:117], v[226:227], v[242:243] op_sel_hi:[1,0,1]
	v_pk_fma_f32 v[118:119], v[118:119], v[226:227], v[244:245] op_sel_hi:[1,0,1]
	v_pk_fma_f32 v[112:113], v[112:113], v[226:227], v[246:247] op_sel_hi:[1,0,1]
	v_pk_fma_f32 v[114:115], v[114:115], v[226:227], v[248:249] op_sel_hi:[1,0,1]
	v_cvt_pk_f16_f32 v116, v116, v117
	v_cvt_pk_f16_f32 v117, v118, v119
	v_cvt_pk_f16_f32 v118, v112, v113
	v_cvt_pk_f16_f32 v119, v114, v115
	v_pk_max_f16 v116, v116, 0
	v_pk_max_f16 v117, v117, 0
	v_pk_max_f16 v118, v118, 0
	v_pk_max_f16 v119, v119, 0
	ds_write_b128 v175, v[116:119] offset:64
	v_mov_b32_e32 v112, v251
	v_mov_b32_e32 v113, v251
	v_mov_b32_e32 v114, v251
	v_mov_b32_e32 v115, v251
	v_mov_b32_e32 v116, v251
	v_mov_b32_e32 v117, v251
	v_mov_b32_e32 v118, v251
	v_mov_b32_e32 v119, v251
	ds_read_b128 v[178:181], v176
	ds_read_b128 v[182:185], v176 offset:1152
	v_pk_fma_f32 v[108:109], v[108:109], v[226:227], v[234:235] op_sel:[0,1,0]
	v_pk_fma_f32 v[110:111], v[110:111], v[226:227], v[236:237] op_sel:[0,1,0]
	v_pk_fma_f32 v[104:105], v[104:105], v[226:227], v[238:239] op_sel:[0,1,0]
	v_pk_fma_f32 v[106:107], v[106:107], v[226:227], v[240:241] op_sel:[0,1,0]
	v_cvt_pk_f16_f32 v108, v108, v109
	v_cvt_pk_f16_f32 v109, v110, v111
	v_cvt_pk_f16_f32 v110, v104, v105
	v_cvt_pk_f16_f32 v111, v106, v107
	v_pk_max_f16 v108, v108, 0
	v_pk_max_f16 v109, v109, 0
	v_pk_max_f16 v110, v110, 0
	v_pk_max_f16 v111, v111, 0
	s_waitcnt lgkmcnt(0)
	s_mul_i32 s34, s10, 0
	buffer_store_dwordx4 v[178:181], v250, s[20:23], s34 offen nt
	s_mul_i32 s35, s10, 16
	buffer_store_dwordx4 v[182:185], v250, s[20:23], s35 offen nt
	ds_write_b128 v175, v[108:111]
	v_mov_b32_e32 v104, v251
	v_mov_b32_e32 v105, v251
	v_mov_b32_e32 v106, v251
	v_mov_b32_e32 v107, v251
	v_mov_b32_e32 v108, v251
	v_mov_b32_e32 v109, v251
	v_mov_b32_e32 v110, v251
	v_mov_b32_e32 v111, v251
	v_pk_fma_f32 v[100:101], v[100:101], v[226:227], v[242:243] op_sel:[0,1,0]
	v_pk_fma_f32 v[102:103], v[102:103], v[226:227], v[244:245] op_sel:[0,1,0]
	v_pk_fma_f32 v[92:93], v[92:93], v[226:227], v[246:247] op_sel:[0,1,0]
	v_pk_fma_f32 v[94:95], v[94:95], v[226:227], v[248:249] op_sel:[0,1,0]
	v_cvt_pk_f16_f32 v100, v100, v101
	v_cvt_pk_f16_f32 v101, v102, v103
	v_cvt_pk_f16_f32 v102, v92, v93
	v_cvt_pk_f16_f32 v103, v94, v95
	v_pk_max_f16 v100, v100, 0
	v_pk_max_f16 v101, v101, 0
	v_pk_max_f16 v102, v102, 0
	v_pk_max_f16 v103, v103, 0
	ds_write_b128 v175, v[100:103] offset:64
	v_mov_b32_e32 v92, v251
	v_mov_b32_e32 v93, v251
	v_mov_b32_e32 v94, v251
	v_mov_b32_e32 v95, v251
	v_mov_b32_e32 v100, v251
	v_mov_b32_e32 v101, v251
	v_mov_b32_e32 v102, v251
	v_mov_b32_e32 v103, v251
	ds_read_b128 v[186:189], v176
	ds_read_b128 v[190:193], v176 offset:1152
	v_pk_fma_f32 v[96:97], v[96:97], v[228:229], v[234:235] op_sel_hi:[1,0,1]
	v_pk_fma_f32 v[98:99], v[98:99], v[228:229], v[236:237] op_sel_hi:[1,0,1]
	v_pk_fma_f32 v[88:89], v[88:89], v[228:229], v[238:239] op_sel_hi:[1,0,1]
	v_pk_fma_f32 v[90:91], v[90:91], v[228:229], v[240:241] op_sel_hi:[1,0,1]
	v_cvt_pk_f16_f32 v96, v96, v97
	v_cvt_pk_f16_f32 v97, v98, v99
	v_cvt_pk_f16_f32 v98, v88, v89
	v_cvt_pk_f16_f32 v99, v90, v91
	v_pk_max_f16 v96, v96, 0
	v_pk_max_f16 v97, v97, 0
	v_pk_max_f16 v98, v98, 0
	v_pk_max_f16 v99, v99, 0
	s_waitcnt lgkmcnt(0)
	s_mul_i32 s34, s10, 32
	buffer_store_dwordx4 v[186:189], v250, s[20:23], s34 offen nt
	s_mul_i32 s35, s10, 48
	buffer_store_dwordx4 v[190:193], v250, s[20:23], s35 offen nt
	ds_write_b128 v175, v[96:99]
	v_mov_b32_e32 v88, v251
	v_mov_b32_e32 v89, v251
	v_mov_b32_e32 v90, v251
	v_mov_b32_e32 v91, v251
	v_mov_b32_e32 v96, v251
	v_mov_b32_e32 v97, v251
	v_mov_b32_e32 v98, v251
	v_mov_b32_e32 v99, v251
	v_pk_fma_f32 v[84:85], v[84:85], v[228:229], v[242:243] op_sel_hi:[1,0,1]
	v_pk_fma_f32 v[86:87], v[86:87], v[228:229], v[244:245] op_sel_hi:[1,0,1]
	v_pk_fma_f32 v[76:77], v[76:77], v[228:229], v[246:247] op_sel_hi:[1,0,1]
	v_pk_fma_f32 v[78:79], v[78:79], v[228:229], v[248:249] op_sel_hi:[1,0,1]
	v_cvt_pk_f16_f32 v84, v84, v85
	v_cvt_pk_f16_f32 v85, v86, v87
	v_cvt_pk_f16_f32 v86, v76, v77
	v_cvt_pk_f16_f32 v87, v78, v79
	v_pk_max_f16 v84, v84, 0
	v_pk_max_f16 v85, v85, 0
	v_pk_max_f16 v86, v86, 0
	v_pk_max_f16 v87, v87, 0
	ds_write_b128 v175, v[84:87] offset:64
	v_mov_b32_e32 v76, v251
	v_mov_b32_e32 v77, v251
	v_mov_b32_e32 v78, v251
	v_mov_b32_e32 v79, v251
	v_mov_b32_e32 v84, v251
	v_mov_b32_e32 v85, v251
	v_mov_b32_e32 v86, v251
	v_mov_b32_e32 v87, v251
	ds_read_b128 v[178:181], v176
	ds_read_b128 v[182:185], v176 offset:1152
	v_pk_fma_f32 v[80:81], v[80:81], v[228:229], v[234:235] op_sel:[0,1,0]
	v_pk_fma_f32 v[82:83], v[82:83], v[228:229], v[236:237] op_sel:[0,1,0]
	v_pk_fma_f32 v[72:73], v[72:73], v[228:229], v[238:239] op_sel:[0,1,0]
	v_pk_fma_f32 v[74:75], v[74:75], v[228:229], v[240:241] op_sel:[0,1,0]
	v_cvt_pk_f16_f32 v80, v80, v81
	v_cvt_pk_f16_f32 v81, v82, v83
	v_cvt_pk_f16_f32 v82, v72, v73
	v_cvt_pk_f16_f32 v83, v74, v75
	v_pk_max_f16 v80, v80, 0
	v_pk_max_f16 v81, v81, 0
	v_pk_max_f16 v82, v82, 0
	v_pk_max_f16 v83, v83, 0
	s_waitcnt lgkmcnt(0)
	s_mul_i32 s34, s10, 64
	buffer_store_dwordx4 v[178:181], v250, s[20:23], s34 offen nt
	s_mul_i32 s35, s10, 80
	buffer_store_dwordx4 v[182:185], v250, s[20:23], s35 offen nt
	ds_write_b128 v175, v[80:83]
	v_mov_b32_e32 v72, v251
	v_mov_b32_e32 v73, v251
	v_mov_b32_e32 v74, v251
	v_mov_b32_e32 v75, v251
	v_mov_b32_e32 v80, v251
	v_mov_b32_e32 v81, v251
	v_mov_b32_e32 v82, v251
	v_mov_b32_e32 v83, v251
	v_pk_fma_f32 v[68:69], v[68:69], v[228:229], v[242:243] op_sel:[0,1,0]
	v_pk_fma_f32 v[70:71], v[70:71], v[228:229], v[244:245] op_sel:[0,1,0]
	v_pk_fma_f32 v[64:65], v[64:65], v[228:229], v[246:247] op_sel:[0,1,0]
	v_pk_fma_f32 v[66:67], v[66:67], v[228:229], v[248:249] op_sel:[0,1,0]
	v_cvt_pk_f16_f32 v68, v68, v69
	v_cvt_pk_f16_f32 v69, v70, v71
	v_cvt_pk_f16_f32 v70, v64, v65
	v_cvt_pk_f16_f32 v71, v66, v67
	v_pk_max_f16 v68, v68, 0
	v_pk_max_f16 v69, v69, 0
	v_pk_max_f16 v70, v70, 0
	v_pk_max_f16 v71, v71, 0
	ds_write_b128 v175, v[68:71] offset:64
	v_mov_b32_e32 v64, v251
	v_mov_b32_e32 v65, v251
	v_mov_b32_e32 v66, v251
	v_mov_b32_e32 v67, v251
	v_mov_b32_e32 v68, v251
	v_mov_b32_e32 v69, v251
	v_mov_b32_e32 v70, v251
	v_mov_b32_e32 v71, v251
	ds_read_b128 v[186:189], v176
	ds_read_b128 v[190:193], v176 offset:1152
	v_pk_fma_f32 v[60:61], v[60:61], v[230:231], v[234:235] op_sel_hi:[1,0,1]
	v_pk_fma_f32 v[62:63], v[62:63], v[230:231], v[236:237] op_sel_hi:[1,0,1]
	v_pk_fma_f32 v[56:57], v[56:57], v[230:231], v[238:239] op_sel_hi:[1,0,1]
	v_pk_fma_f32 v[58:59], v[58:59], v[230:231], v[240:241] op_sel_hi:[1,0,1]
	v_cvt_pk_f16_f32 v60, v60, v61
	v_cvt_pk_f16_f32 v61, v62, v63
	v_cvt_pk_f16_f32 v62, v56, v57
	v_cvt_pk_f16_f32 v63, v58, v59
	v_pk_max_f16 v60, v60, 0
	v_pk_max_f16 v61, v61, 0
	v_pk_max_f16 v62, v62, 0
	v_pk_max_f16 v63, v63, 0
	s_waitcnt lgkmcnt(0)
	s_mul_i32 s34, s10, 96
	buffer_store_dwordx4 v[186:189], v250, s[20:23], s34 offen nt
	s_mul_i32 s35, s10, 112
	buffer_store_dwordx4 v[190:193], v250, s[20:23], s35 offen nt
	ds_write_b128 v175, v[60:63]
	v_mov_b32_e32 v56, v251
	v_mov_b32_e32 v57, v251
	v_mov_b32_e32 v58, v251
	v_mov_b32_e32 v59, v251
	v_mov_b32_e32 v60, v251
	v_mov_b32_e32 v61, v251
	v_mov_b32_e32 v62, v251
	v_mov_b32_e32 v63, v251
	v_pk_fma_f32 v[52:53], v[52:53], v[230:231], v[242:243] op_sel_hi:[1,0,1]
	v_pk_fma_f32 v[54:55], v[54:55], v[230:231], v[244:245] op_sel_hi:[1,0,1]
	v_pk_fma_f32 v[44:45], v[44:45], v[230:231], v[246:247] op_sel_hi:[1,0,1]
	v_pk_fma_f32 v[46:47], v[46:47], v[230:231], v[248:249] op_sel_hi:[1,0,1]
	v_cvt_pk_f16_f32 v52, v52, v53
	v_cvt_pk_f16_f32 v53, v54, v55
	v_cvt_pk_f16_f32 v54, v44, v45
	v_cvt_pk_f16_f32 v55, v46, v47
	v_pk_max_f16 v52, v52, 0
	v_pk_max_f16 v53, v53, 0
	v_pk_max_f16 v54, v54, 0
	v_pk_max_f16 v55, v55, 0
	ds_write_b128 v175, v[52:55] offset:64
	v_mov_b32_e32 v44, v251
	v_mov_b32_e32 v45, v251
	v_mov_b32_e32 v46, v251
	v_mov_b32_e32 v47, v251
	v_mov_b32_e32 v52, v251
	v_mov_b32_e32 v53, v251
	v_mov_b32_e32 v54, v251
	v_mov_b32_e32 v55, v251
	ds_read_b128 v[178:181], v176
	ds_read_b128 v[182:185], v176 offset:1152
	v_pk_fma_f32 v[48:49], v[48:49], v[230:231], v[234:235] op_sel:[0,1,0]
	v_pk_fma_f32 v[50:51], v[50:51], v[230:231], v[236:237] op_sel:[0,1,0]
	v_pk_fma_f32 v[40:41], v[40:41], v[230:231], v[238:239] op_sel:[0,1,0]
	v_pk_fma_f32 v[42:43], v[42:43], v[230:231], v[240:241] op_sel:[0,1,0]
	v_cvt_pk_f16_f32 v48, v48, v49
	v_cvt_pk_f16_f32 v49, v50, v51
	v_cvt_pk_f16_f32 v50, v40, v41
	v_cvt_pk_f16_f32 v51, v42, v43
	v_pk_max_f16 v48, v48, 0
	v_pk_max_f16 v49, v49, 0
	v_pk_max_f16 v50, v50, 0
	v_pk_max_f16 v51, v51, 0
	s_waitcnt lgkmcnt(0)
	s_mul_i32 s34, s10, 256
	buffer_store_dwordx4 v[178:181], v250, s[20:23], s34 offen nt
	s_mul_i32 s35, s10, 272
	buffer_store_dwordx4 v[182:185], v250, s[20:23], s35 offen nt
	ds_write_b128 v175, v[48:51]
	v_mov_b32_e32 v40, v251
	v_mov_b32_e32 v41, v251
	v_mov_b32_e32 v42, v251
	v_mov_b32_e32 v43, v251
	v_mov_b32_e32 v48, v251
	v_mov_b32_e32 v49, v251
	v_mov_b32_e32 v50, v251
	v_mov_b32_e32 v51, v251
	v_pk_fma_f32 v[36:37], v[36:37], v[230:231], v[242:243] op_sel:[0,1,0]
	v_pk_fma_f32 v[38:39], v[38:39], v[230:231], v[244:245] op_sel:[0,1,0]
	v_pk_fma_f32 v[28:29], v[28:29], v[230:231], v[246:247] op_sel:[0,1,0]
	v_pk_fma_f32 v[30:31], v[30:31], v[230:231], v[248:249] op_sel:[0,1,0]
	v_cvt_pk_f16_f32 v36, v36, v37
	v_cvt_pk_f16_f32 v37, v38, v39
	v_cvt_pk_f16_f32 v38, v28, v29
	v_cvt_pk_f16_f32 v39, v30, v31
	v_pk_max_f16 v36, v36, 0
	v_pk_max_f16 v37, v37, 0
	v_pk_max_f16 v38, v38, 0
	v_pk_max_f16 v39, v39, 0
	ds_write_b128 v175, v[36:39] offset:64
	v_mov_b32_e32 v28, v251
	v_mov_b32_e32 v29, v251
	v_mov_b32_e32 v30, v251
	v_mov_b32_e32 v31, v251
	v_mov_b32_e32 v36, v251
	v_mov_b32_e32 v37, v251
	v_mov_b32_e32 v38, v251
	v_mov_b32_e32 v39, v251
	ds_read_b128 v[186:189], v176
	ds_read_b128 v[190:193], v176 offset:1152
	v_pk_fma_f32 v[32:33], v[32:33], v[232:233], v[234:235] op_sel_hi:[1,0,1]
	v_pk_fma_f32 v[34:35], v[34:35], v[232:233], v[236:237] op_sel_hi:[1,0,1]
	v_pk_fma_f32 v[24:25], v[24:25], v[232:233], v[238:239] op_sel_hi:[1,0,1]
	v_pk_fma_f32 v[26:27], v[26:27], v[232:233], v[240:241] op_sel_hi:[1,0,1]
	v_cvt_pk_f16_f32 v32, v32, v33
	v_cvt_pk_f16_f32 v33, v34, v35
	v_cvt_pk_f16_f32 v34, v24, v25
	v_cvt_pk_f16_f32 v35, v26, v27
	v_pk_max_f16 v32, v32, 0
	v_pk_max_f16 v33, v33, 0
	v_pk_max_f16 v34, v34, 0
	v_pk_max_f16 v35, v35, 0
	s_waitcnt lgkmcnt(0)
	s_mul_i32 s34, s10, 288
	buffer_store_dwordx4 v[186:189], v250, s[20:23], s34 offen nt
	s_mul_i32 s35, s10, 304
	buffer_store_dwordx4 v[190:193], v250, s[20:23], s35 offen nt
	ds_write_b128 v175, v[32:35]
	v_mov_b32_e32 v24, v251
	v_mov_b32_e32 v25, v251
	v_mov_b32_e32 v26, v251
	v_mov_b32_e32 v27, v251
	v_mov_b32_e32 v32, v251
	v_mov_b32_e32 v33, v251
	v_mov_b32_e32 v34, v251
	v_mov_b32_e32 v35, v251
	v_pk_fma_f32 v[20:21], v[20:21], v[232:233], v[242:243] op_sel_hi:[1,0,1]
	v_pk_fma_f32 v[22:23], v[22:23], v[232:233], v[244:245] op_sel_hi:[1,0,1]
	v_pk_fma_f32 v[12:13], v[12:13], v[232:233], v[246:247] op_sel_hi:[1,0,1]
	v_pk_fma_f32 v[14:15], v[14:15], v[232:233], v[248:249] op_sel_hi:[1,0,1]
	v_cvt_pk_f16_f32 v20, v20, v21
	v_cvt_pk_f16_f32 v21, v22, v23
	v_cvt_pk_f16_f32 v22, v12, v13
	v_cvt_pk_f16_f32 v23, v14, v15
	v_pk_max_f16 v20, v20, 0
	v_pk_max_f16 v21, v21, 0
	v_pk_max_f16 v22, v22, 0
	v_pk_max_f16 v23, v23, 0
	ds_write_b128 v175, v[20:23] offset:64
	v_mov_b32_e32 v12, v251
	v_mov_b32_e32 v13, v251
	v_mov_b32_e32 v14, v251
	v_mov_b32_e32 v15, v251
	v_mov_b32_e32 v20, v251
	v_mov_b32_e32 v21, v251
	v_mov_b32_e32 v22, v251
	v_mov_b32_e32 v23, v251
	ds_read_b128 v[178:181], v176
	ds_read_b128 v[182:185], v176 offset:1152
	v_pk_fma_f32 v[16:17], v[16:17], v[232:233], v[234:235] op_sel:[0,1,0]
	v_pk_fma_f32 v[18:19], v[18:19], v[232:233], v[236:237] op_sel:[0,1,0]
	v_pk_fma_f32 v[8:9], v[8:9], v[232:233], v[238:239] op_sel:[0,1,0]
	v_pk_fma_f32 v[10:11], v[10:11], v[232:233], v[240:241] op_sel:[0,1,0]
	v_cvt_pk_f16_f32 v16, v16, v17
	v_cvt_pk_f16_f32 v17, v18, v19
	v_cvt_pk_f16_f32 v18, v8, v9
	v_cvt_pk_f16_f32 v19, v10, v11
	v_pk_max_f16 v16, v16, 0
	v_pk_max_f16 v17, v17, 0
	v_pk_max_f16 v18, v18, 0
	v_pk_max_f16 v19, v19, 0
	s_waitcnt lgkmcnt(0)
	s_mul_i32 s34, s10, 320
	buffer_store_dwordx4 v[178:181], v250, s[20:23], s34 offen nt
	s_mul_i32 s35, s10, 336
	buffer_store_dwordx4 v[182:185], v250, s[20:23], s35 offen nt
	ds_write_b128 v175, v[16:19]
	v_mov_b32_e32 v8, v251
	v_mov_b32_e32 v9, v251
	v_mov_b32_e32 v10, v251
	v_mov_b32_e32 v11, v251
	v_mov_b32_e32 v16, v251
	v_mov_b32_e32 v17, v251
	v_mov_b32_e32 v18, v251
	v_mov_b32_e32 v19, v251
	v_pk_fma_f32 v[4:5], v[4:5], v[232:233], v[242:243] op_sel:[0,1,0]
	v_pk_fma_f32 v[6:7], v[6:7], v[232:233], v[244:245] op_sel:[0,1,0]
	v_pk_fma_f32 v[0:1], v[0:1], v[232:233], v[246:247] op_sel:[0,1,0]
	v_pk_fma_f32 v[2:3], v[2:3], v[232:233], v[248:249] op_sel:[0,1,0]
	v_cvt_pk_f16_f32 v4, v4, v5
	v_cvt_pk_f16_f32 v5, v6, v7
	v_cvt_pk_f16_f32 v6, v0, v1
	v_cvt_pk_f16_f32 v7, v2, v3
	v_pk_max_f16 v4, v4, 0
	v_pk_max_f16 v5, v5, 0
	v_pk_max_f16 v6, v6, 0
	v_pk_max_f16 v7, v7, 0
	ds_write_b128 v175, v[4:7] offset:64
	v_mov_b32_e32 v0, v251
	v_mov_b32_e32 v1, v251
	v_mov_b32_e32 v2, v251
	v_mov_b32_e32 v3, v251
	v_mov_b32_e32 v4, v251
	v_mov_b32_e32 v5, v251
	v_mov_b32_e32 v6, v251
	v_mov_b32_e32 v7, v251
	ds_read_b128 v[186:189], v176
	ds_read_b128 v[190:193], v176 offset:1152
	s_waitcnt lgkmcnt(0)
	s_mul_i32 s34, s10, 352
	buffer_store_dwordx4 v[186:189], v250, s[20:23], s34 offen nt
	s_mul_i32 s35, s10, 368
	buffer_store_dwordx4 v[190:193], v250, s[20:23], s35 offen nt
	s_mov_b32 s68, s67
	s_mov_b32 s70, s69
	s_mov_b64 s[30:31], s[0:1]
	s_mov_b64 s[28:29], s[8:9]
	s_mov_b64 vcc, s[6:7]
	s_cbranch_vccz .LBB9_12
	s_waitcnt vmcnt(0)
	s_cmpk_gt_u32 s36, 0xff
	s_cbranch_scc1 .LBB9_31
	s_barrier
